# GEMM epilogue stores (down-proj both layers, QKV layer 0, Wo both layers) staged through an LDS exchange: 4 rows x 256 B per store instruction instead of 16 rows x 64 B
# speedup vs baseline: 1.0053x; 1.0053x over previous
.LBB0_171:
	v_lshrrev_b32_e32 v4, 1, v198
	s_add_u32 s60, s16, 0x25b00000
	v_and_b32_e32 v4, 24, v4
	s_addc_u32 s61, s17, 0
	v_and_b32_e32 v2, 15, v198
	v_lshlrev_b32_e32 v5, 1, v4
	s_add_u32 s16, s10, 0x80
	v_lshl_or_b32 v201, s20, 6, v2
	v_lshl_or_b32 v2, v2, 6, v5
	v_lshlrev_b32_e32 v5, 2, v198
	s_addc_u32 s17, s11, 0
	s_lshl_b32 s20, s20, 13
	v_and_b32_e32 v5, 32, v5
	v_bitop3_b32 v9, v2, s20, v5 bitop3:0xde
	s_lshl_b32 s20, s38, 5
	s_and_b32 s20, s20, 0x60
	s_lshl_b32 s38, s20, 7
	v_bitop3_b32 v2, v2, s38, v5 bitop3:0xde
	s_add_u32 s38, s12, 0x80
	s_waitcnt vmcnt(2)
	s_barrier
	s_addc_u32 s39, s13, 0
	s_add_i32 s62, s56, 0x18000
	s_mov_b32 s40, m0
	s_mov_b32 m0, s62
	s_nop 0
	global_load_lds_dwordx4 v199, s[38:39]
	s_mov_b32 m0, s40
	s_add_i32 s63, s56, 0x1a000
	s_mov_b32 s40, m0
	s_mov_b32 m0, s63
	s_nop 0
	global_load_lds_dwordx4 v200, s[38:39]
	s_mov_b32 m0, s40
	s_add_i32 s64, s56, 0x8000
	s_mov_b32 s38, m0
	s_mov_b32 m0, s64
	s_nop 0
	global_load_lds_dwordx4 v220, s[16:17]
	s_mov_b32 m0, s38
	s_add_i32 s65, s56, 0xa000
	s_mov_b32 s38, m0
	s_mov_b32 m0, s65
	s_nop 0
	global_load_lds_dwordx4 v222, s[16:17]
	s_mov_b32 m0, s38
	s_add_u32 s16, s12, 0x20080
	s_addc_u32 s17, s13, 0
	s_add_i32 s66, s56, 0x1c000
	s_mov_b32 s38, m0
	s_mov_b32 m0, s66
	s_nop 0
	global_load_lds_dwordx4 v199, s[16:17]
	s_mov_b32 m0, s38
	s_add_i32 s67, s56, 0x1e000
	s_mov_b32 s38, m0
	s_mov_b32 m0, s67
	s_nop 0
	global_load_lds_dwordx4 v200, s[16:17]
	s_mov_b32 m0, s38
	s_waitcnt vmcnt(6)
	s_add_i32 s38, s56, 0xc000
	s_cmpk_lt_u32 s18, 0x100
	v_add_u32_e32 v203, 0, v2
	s_cselect_b64 s[16:17], -1, 0
	v_or_b32_e32 v202, s20, v4
	v_add_u32_e32 v204, 0x10000, v203
	v_add_u32_e32 v205, 0x14000, v203
	v_add_u32_e32 v206, 0, v9
	v_mov_b32_e32 v207, s38
	v_mov_b32_e32 v209, s56
	v_mov_b32_e32 v210, s9
	v_mov_b32_e32 v211, s21
	v_mov_b32_e32 v212, s28
	v_mov_b32_e32 v213, s29
	s_movk_i32 s68, 0xc4
	v_mov_b32_e32 v195, 0
	s_mov_b32 s18, 0x3d000000
	s_mov_b64 s[20:21], 0x40000
	s_mov_b32 s69, 0x40000
	s_mov_b64 s[28:29], 0x48000
	s_mov_b32 s70, 0x48000
	s_mov_b64 s[38:39], 0x50000
	s_mov_b32 s71, 0x50000
	s_mov_b64 s[40:41], 0x58000
	s_mov_b32 s72, 0x58000
	v_mov_b64_e32 v[196:197], 0x617
	v_mov_b32_e32 v214, 1
	v_mov_b32_e32 v215, 0x3e38aa3b
	s_barrier
	v_and_b32_e32 v250, 63, v0
	v_and_b32_e32 v251, 15, v250
	v_lshrrev_b32_e32 v252, 4, v250
	v_readfirstlane_b32 s99, v0
	s_lshr_b32 s99, s99, 6
	s_and_b32 s100, s99, 3
	s_lshr_b32 s101, s99, 2
	s_lshl_b32 s100, s100, 2
	v_add_u32_e32 v253, s100, v252
	v_xor_b32_e32 v254, v253, v251
	s_lshl_b32 s101, s101, 12
	s_add_i32 s101, s101, 0xc000
	v_lshlrev_b32_e32 v240, 8, v251
	v_lshl_add_u32 v240, v254, 4, v240
	v_add_u32_e32 v240, s101, v240
	v_lshlrev_b32_e32 v241, 8, v253
	v_lshl_add_u32 v241, v254, 4, v241
	v_add_u32_e32 v241, s101, v241
	v_sub_u32_e32 v242, v253, v251
	v_lshlrev_b32_e32 v242, 11, v242
	v_lshl_add_u32 v242, v251, 4, v242
	v_lshlrev_b32_e32 v244, 4, v253
	v_sub_u32_e32 v242, v242, v244
	v_ashrrev_i32_e32 v243, 31, v242
	s_branch .LBB0_174

.LBB0_195:
	s_ashr_i32 s9, s74, 2
	s_lshl_b32 s44, s74, 8
	s_and_b32 s46, s44, 0x300
	s_mul_hi_i32 s45, s9, 0x4100000
	s_mul_i32 s9, s9, 0x4100000
	s_add_u32 s44, s60, s9
	s_addc_u32 s45, s61, s45
	s_cmp_lt_u32 s74, 4
	s_cselect_b64 vcc, -1, 0
	v_lshl_add_u32 v14, s73, 8, v201
	v_or_b32_e32 v4, s46, v202
	v_cndmask_b32_e32 v2, 1.0, v215, vcc
	v_lshlrev_b32_e32 v194, 1, v4
	v_ashrrev_i32_e32 v15, 31, v14
	v_pk_mul_f32 v[10:11], v[192:193], s[18:19] op_sel_hi:[1,0]
	v_pk_mul_f32 v[12:13], v[190:191], s[18:19] op_sel_hi:[1,0]
	v_pk_mul_f32 v[20:21], v[186:187], s[18:19] op_sel_hi:[1,0]
	v_lshl_add_u64 v[16:17], s[44:45], 0, v[194:195]
	v_lshlrev_b64 v[4:5], 11, v[14:15]
	v_pk_mul_f32 v[18:19], v[188:189], s[18:19] op_sel_hi:[1,0]
	v_pk_mul_f32 v[22:23], v[2:3], v[10:11] op_sel_hi:[0,1]
	v_pk_mul_f32 v[10:11], v[2:3], v[12:13] op_sel_hi:[0,1]
	v_pk_mul_f32 v[12:13], v[2:3], v[20:21] op_sel_hi:[0,1]
	v_lshl_add_u64 v[4:5], v[16:17], 0, v[4:5]
	v_pk_mul_f32 v[18:19], v[2:3], v[18:19] op_sel_hi:[0,1]
	v_cvt_pk_bf16_f32 v10, v10, v11
	v_cvt_pk_bf16_f32 v11, v22, v23
	v_cvt_pk_bf16_f32 v12, v12, v13
	v_cvt_pk_bf16_f32 v13, v18, v19
	ds_write_b128 v240, v[10:13]
	s_waitcnt lgkmcnt(0)
	s_barrier
	ds_read_b128 v[246:249], v241
	v_lshl_add_u64 v[244:245], v[4:5], 0, v[242:243]
	s_waitcnt lgkmcnt(0)
	global_store_dwordx4 v[244:245], v[246:249], off
	v_pk_mul_f32 v[20:21], v[178:179], s[18:19] op_sel_hi:[1,0]
	v_pk_mul_f32 v[18:19], v[180:181], s[18:19] op_sel_hi:[1,0]
	v_pk_mul_f32 v[10:11], v[184:185], s[18:19] op_sel_hi:[1,0]
	v_pk_mul_f32 v[12:13], v[182:183], s[18:19] op_sel_hi:[1,0]
	v_pk_mul_f32 v[22:23], v[2:3], v[10:11] op_sel_hi:[0,1]
	v_pk_mul_f32 v[10:11], v[2:3], v[12:13] op_sel_hi:[0,1]
	v_pk_mul_f32 v[12:13], v[2:3], v[20:21] op_sel_hi:[0,1]
	v_cvt_pk_bf16_f32 v10, v10, v11
	v_pk_mul_f32 v[18:19], v[2:3], v[18:19] op_sel_hi:[0,1]
	v_cvt_pk_bf16_f32 v11, v22, v23
	v_cvt_pk_bf16_f32 v12, v12, v13
	v_cvt_pk_bf16_f32 v13, v18, v19
	ds_write_b128 v240, v[10:13] offset:8192
	s_waitcnt lgkmcnt(0)
	s_barrier
	ds_read_b128 v[246:249], v241 offset:8192
	v_lshl_add_u64 v[244:245], v[4:5], 0, v[242:243]
	s_waitcnt lgkmcnt(0)
	global_store_dwordx4 v[244:245], v[246:249], off offset:256
	v_pk_mul_f32 v[22:23], v[170:171], s[18:19] op_sel_hi:[1,0]
	v_pk_mul_f32 v[20:21], v[172:173], s[18:19] op_sel_hi:[1,0]
	v_or_b32_e32 v10, 16, v14
	v_ashrrev_i32_e32 v11, 31, v10
	v_lshlrev_b64 v[10:11], 11, v[10:11]
	v_lshl_add_u64 v[18:19], v[16:17], 0, v[10:11]
	v_pk_mul_f32 v[10:11], v[176:177], s[18:19] op_sel_hi:[1,0]
	v_pk_mul_f32 v[12:13], v[174:175], s[18:19] op_sel_hi:[1,0]
	v_pk_mul_f32 v[24:25], v[2:3], v[10:11] op_sel_hi:[0,1]
	v_pk_mul_f32 v[10:11], v[2:3], v[12:13] op_sel_hi:[0,1]
	v_pk_mul_f32 v[12:13], v[2:3], v[22:23] op_sel_hi:[0,1]
	v_pk_mul_f32 v[20:21], v[2:3], v[20:21] op_sel_hi:[0,1]
	v_cvt_pk_bf16_f32 v10, v10, v11
	v_cvt_pk_bf16_f32 v11, v24, v25
	v_cvt_pk_bf16_f32 v12, v12, v13
	v_cvt_pk_bf16_f32 v13, v20, v21
	ds_write_b128 v240, v[10:13]
	s_waitcnt lgkmcnt(0)
	s_barrier
	ds_read_b128 v[246:249], v241
	v_lshl_add_u64 v[244:245], v[18:19], 0, v[242:243]
	s_waitcnt lgkmcnt(0)
	global_store_dwordx4 v[244:245], v[246:249], off
	v_pk_mul_f32 v[22:23], v[162:163], s[18:19] op_sel_hi:[1,0]
	v_pk_mul_f32 v[20:21], v[164:165], s[18:19] op_sel_hi:[1,0]
	v_pk_mul_f32 v[10:11], v[168:169], s[18:19] op_sel_hi:[1,0]
	v_pk_mul_f32 v[12:13], v[166:167], s[18:19] op_sel_hi:[1,0]
	v_pk_mul_f32 v[24:25], v[2:3], v[10:11] op_sel_hi:[0,1]
	v_pk_mul_f32 v[10:11], v[2:3], v[12:13] op_sel_hi:[0,1]
	v_pk_mul_f32 v[12:13], v[2:3], v[22:23] op_sel_hi:[0,1]
	v_cvt_pk_bf16_f32 v10, v10, v11
	v_pk_mul_f32 v[20:21], v[2:3], v[20:21] op_sel_hi:[0,1]
	v_cvt_pk_bf16_f32 v11, v24, v25
	v_cvt_pk_bf16_f32 v12, v12, v13
	v_cvt_pk_bf16_f32 v13, v20, v21
	ds_write_b128 v240, v[10:13] offset:8192
	s_waitcnt lgkmcnt(0)
	s_barrier
	ds_read_b128 v[246:249], v241 offset:8192
	v_lshl_add_u64 v[244:245], v[18:19], 0, v[242:243]
	s_waitcnt lgkmcnt(0)
	global_store_dwordx4 v[244:245], v[246:249], off offset:256
	v_pk_mul_f32 v[22:23], v[154:155], s[18:19] op_sel_hi:[1,0]
	v_pk_mul_f32 v[20:21], v[156:157], s[18:19] op_sel_hi:[1,0]
	v_or_b32_e32 v10, 32, v14
	v_ashrrev_i32_e32 v11, 31, v10
	v_lshlrev_b64 v[10:11], 11, v[10:11]
	v_lshl_add_u64 v[18:19], v[16:17], 0, v[10:11]
	v_pk_mul_f32 v[10:11], v[160:161], s[18:19] op_sel_hi:[1,0]
	v_pk_mul_f32 v[12:13], v[158:159], s[18:19] op_sel_hi:[1,0]
	v_pk_mul_f32 v[24:25], v[2:3], v[10:11] op_sel_hi:[0,1]
	v_pk_mul_f32 v[10:11], v[2:3], v[12:13] op_sel_hi:[0,1]
	v_pk_mul_f32 v[12:13], v[2:3], v[22:23] op_sel_hi:[0,1]
	v_pk_mul_f32 v[20:21], v[2:3], v[20:21] op_sel_hi:[0,1]
	v_cvt_pk_bf16_f32 v10, v10, v11
	v_cvt_pk_bf16_f32 v11, v24, v25
	v_cvt_pk_bf16_f32 v12, v12, v13
	v_cvt_pk_bf16_f32 v13, v20, v21
	ds_write_b128 v240, v[10:13]
	s_waitcnt lgkmcnt(0)
	s_barrier
	ds_read_b128 v[246:249], v241
	v_lshl_add_u64 v[244:245], v[18:19], 0, v[242:243]
	s_waitcnt lgkmcnt(0)
	global_store_dwordx4 v[244:245], v[246:249], off
	v_pk_mul_f32 v[22:23], v[146:147], s[18:19] op_sel_hi:[1,0]
	v_pk_mul_f32 v[20:21], v[148:149], s[18:19] op_sel_hi:[1,0]
	v_pk_mul_f32 v[10:11], v[152:153], s[18:19] op_sel_hi:[1,0]
	v_pk_mul_f32 v[12:13], v[150:151], s[18:19] op_sel_hi:[1,0]
	v_pk_mul_f32 v[24:25], v[2:3], v[10:11] op_sel_hi:[0,1]
	v_pk_mul_f32 v[10:11], v[2:3], v[12:13] op_sel_hi:[0,1]
	v_pk_mul_f32 v[12:13], v[2:3], v[22:23] op_sel_hi:[0,1]
	v_cvt_pk_bf16_f32 v10, v10, v11
	v_pk_mul_f32 v[20:21], v[2:3], v[20:21] op_sel_hi:[0,1]
	v_cvt_pk_bf16_f32 v11, v24, v25
	v_cvt_pk_bf16_f32 v12, v12, v13
	v_cvt_pk_bf16_f32 v13, v20, v21
	ds_write_b128 v240, v[10:13] offset:8192
	s_waitcnt lgkmcnt(0)
	s_barrier
	ds_read_b128 v[246:249], v241 offset:8192
	v_lshl_add_u64 v[244:245], v[18:19], 0, v[242:243]
	s_waitcnt lgkmcnt(0)
	global_store_dwordx4 v[244:245], v[246:249], off offset:256
	v_pk_mul_f32 v[18:19], v[138:139], s[18:19] op_sel_hi:[1,0]
	s_nop 0
	v_or_b32_e32 v10, 48, v14
	v_ashrrev_i32_e32 v11, 31, v10
	v_lshlrev_b64 v[10:11], 11, v[10:11]
	v_lshl_add_u64 v[14:15], v[16:17], 0, v[10:11]
	v_pk_mul_f32 v[10:11], v[144:145], s[18:19] op_sel_hi:[1,0]
	v_pk_mul_f32 v[12:13], v[142:143], s[18:19] op_sel_hi:[1,0]
	v_pk_mul_f32 v[16:17], v[140:141], s[18:19] op_sel_hi:[1,0]
	v_pk_mul_f32 v[20:21], v[2:3], v[10:11] op_sel_hi:[0,1]
	v_pk_mul_f32 v[10:11], v[2:3], v[12:13] op_sel_hi:[0,1]
	v_pk_mul_f32 v[12:13], v[2:3], v[18:19] op_sel_hi:[0,1]
	v_pk_mul_f32 v[16:17], v[2:3], v[16:17] op_sel_hi:[0,1]
	v_cvt_pk_bf16_f32 v10, v10, v11
	v_cvt_pk_bf16_f32 v11, v20, v21
	v_cvt_pk_bf16_f32 v12, v12, v13
	v_cvt_pk_bf16_f32 v13, v16, v17
	ds_write_b128 v240, v[10:13]
	s_waitcnt lgkmcnt(0)
	s_barrier
	ds_read_b128 v[246:249], v241
	v_lshl_add_u64 v[244:245], v[14:15], 0, v[242:243]
	s_waitcnt lgkmcnt(0)
	global_store_dwordx4 v[244:245], v[246:249], off
	v_pk_mul_f32 v[18:19], v[130:131], s[18:19] op_sel_hi:[1,0]
	v_pk_mul_f32 v[16:17], v[132:133], s[18:19] op_sel_hi:[1,0]
	v_pk_mul_f32 v[10:11], v[136:137], s[18:19] op_sel_hi:[1,0]
	v_pk_mul_f32 v[12:13], v[134:135], s[18:19] op_sel_hi:[1,0]
	v_pk_mul_f32 v[20:21], v[2:3], v[10:11] op_sel_hi:[0,1]
	v_pk_mul_f32 v[10:11], v[2:3], v[12:13] op_sel_hi:[0,1]
	v_pk_mul_f32 v[12:13], v[2:3], v[18:19] op_sel_hi:[0,1]
	v_pk_mul_f32 v[16:17], v[2:3], v[16:17] op_sel_hi:[0,1]
	v_cvt_pk_bf16_f32 v10, v10, v11
	v_cvt_pk_bf16_f32 v11, v20, v21
	v_cvt_pk_bf16_f32 v12, v12, v13
	v_cvt_pk_bf16_f32 v13, v16, v17
	ds_write_b128 v240, v[10:13] offset:8192
	s_waitcnt lgkmcnt(0)
	s_barrier
	ds_read_b128 v[246:249], v241 offset:8192
	v_lshl_add_u64 v[244:245], v[14:15], 0, v[242:243]
	s_waitcnt lgkmcnt(0)
	global_store_dwordx4 v[244:245], v[246:249], off offset:256
	v_pk_mul_f32 v[16:17], v[124:125], s[18:19] op_sel_hi:[1,0]
	v_pk_mul_f32 v[18:19], v[122:123], s[18:19] op_sel_hi:[1,0]
	v_pk_mul_f32 v[10:11], v[128:129], s[18:19] op_sel_hi:[1,0]
	v_pk_mul_f32 v[12:13], v[126:127], s[18:19] op_sel_hi:[1,0]
	v_pk_mul_f32 v[20:21], v[2:3], v[10:11] op_sel_hi:[0,1]
	v_pk_mul_f32 v[10:11], v[2:3], v[12:13] op_sel_hi:[0,1]
	v_pk_mul_f32 v[16:17], v[2:3], v[16:17] op_sel_hi:[0,1]
	v_pk_mul_f32 v[12:13], v[2:3], v[18:19] op_sel_hi:[0,1]
	v_cvt_pk_bf16_f32 v10, v10, v11
	v_cvt_pk_bf16_f32 v11, v20, v21
	v_cvt_pk_bf16_f32 v12, v12, v13
	v_cvt_pk_bf16_f32 v13, v16, v17
	v_add_co_u32_e32 v16, vcc, s69, v4
	v_pk_mul_f32 v[18:19], v[110:111], s[18:19] op_sel_hi:[1,0]
	s_nop 0
	v_addc_co_u32_e32 v17, vcc, 0, v5, vcc
	ds_write_b128 v240, v[10:13]
	s_waitcnt lgkmcnt(0)
	s_barrier
	ds_read_b128 v[246:249], v241
	v_lshl_add_u64 v[244:245], v[16:17], 0, v[242:243]
	s_waitcnt lgkmcnt(0)
	global_store_dwordx4 v[244:245], v[246:249], off
	v_pk_mul_f32 v[16:17], v[112:113], s[18:19] op_sel_hi:[1,0]
	v_lshl_add_u64 v[14:15], v[4:5], 0, s[20:21]
	v_pk_mul_f32 v[10:11], v[120:121], s[18:19] op_sel_hi:[1,0]
	v_pk_mul_f32 v[12:13], v[118:119], s[18:19] op_sel_hi:[1,0]
	v_pk_mul_f32 v[20:21], v[2:3], v[10:11] op_sel_hi:[0,1]
	v_pk_mul_f32 v[10:11], v[2:3], v[12:13] op_sel_hi:[0,1]
	v_pk_mul_f32 v[12:13], v[2:3], v[18:19] op_sel_hi:[0,1]
	v_pk_mul_f32 v[16:17], v[2:3], v[16:17] op_sel_hi:[0,1]
	v_cvt_pk_bf16_f32 v10, v10, v11
	v_cvt_pk_bf16_f32 v11, v20, v21
	v_cvt_pk_bf16_f32 v12, v12, v13
	v_cvt_pk_bf16_f32 v13, v16, v17
	ds_write_b128 v240, v[10:13] offset:8192
	s_waitcnt lgkmcnt(0)
	s_barrier
	ds_read_b128 v[246:249], v241 offset:8192
	v_lshl_add_u64 v[244:245], v[14:15], 0, v[242:243]
	s_waitcnt lgkmcnt(0)
	global_store_dwordx4 v[244:245], v[246:249], off offset:256
	v_pk_mul_f32 v[16:17], v[108:109], s[18:19] op_sel_hi:[1,0]
	v_pk_mul_f32 v[18:19], v[106:107], s[18:19] op_sel_hi:[1,0]
	v_pk_mul_f32 v[10:11], v[116:117], s[18:19] op_sel_hi:[1,0]
	v_pk_mul_f32 v[12:13], v[114:115], s[18:19] op_sel_hi:[1,0]
	v_pk_mul_f32 v[20:21], v[2:3], v[10:11] op_sel_hi:[0,1]
	v_pk_mul_f32 v[10:11], v[2:3], v[12:13] op_sel_hi:[0,1]
	v_pk_mul_f32 v[16:17], v[2:3], v[16:17] op_sel_hi:[0,1]
	v_pk_mul_f32 v[12:13], v[2:3], v[18:19] op_sel_hi:[0,1]
	v_cvt_pk_bf16_f32 v10, v10, v11
	v_cvt_pk_bf16_f32 v11, v20, v21
	v_cvt_pk_bf16_f32 v12, v12, v13
	v_cvt_pk_bf16_f32 v13, v16, v17
	v_add_co_u32_e32 v16, vcc, s70, v4
	v_pk_mul_f32 v[18:19], v[94:95], s[18:19] op_sel_hi:[1,0]
	s_nop 0
	v_addc_co_u32_e32 v17, vcc, 0, v5, vcc
	ds_write_b128 v240, v[10:13]
	s_waitcnt lgkmcnt(0)
	s_barrier
	ds_read_b128 v[246:249], v241
	v_lshl_add_u64 v[244:245], v[16:17], 0, v[242:243]
	s_waitcnt lgkmcnt(0)
	global_store_dwordx4 v[244:245], v[246:249], off
	v_pk_mul_f32 v[16:17], v[96:97], s[18:19] op_sel_hi:[1,0]
	v_lshl_add_u64 v[14:15], v[4:5], 0, s[28:29]
	v_pk_mul_f32 v[10:11], v[104:105], s[18:19] op_sel_hi:[1,0]
	v_pk_mul_f32 v[12:13], v[102:103], s[18:19] op_sel_hi:[1,0]
	v_pk_mul_f32 v[20:21], v[2:3], v[10:11] op_sel_hi:[0,1]
	v_pk_mul_f32 v[10:11], v[2:3], v[12:13] op_sel_hi:[0,1]
	v_pk_mul_f32 v[12:13], v[2:3], v[18:19] op_sel_hi:[0,1]
	v_pk_mul_f32 v[16:17], v[2:3], v[16:17] op_sel_hi:[0,1]
	v_cvt_pk_bf16_f32 v10, v10, v11
	v_cvt_pk_bf16_f32 v11, v20, v21
	v_cvt_pk_bf16_f32 v12, v12, v13
	v_cvt_pk_bf16_f32 v13, v16, v17
	ds_write_b128 v240, v[10:13] offset:8192
	s_waitcnt lgkmcnt(0)
	s_barrier
	ds_read_b128 v[246:249], v241 offset:8192
	v_lshl_add_u64 v[244:245], v[14:15], 0, v[242:243]
	s_waitcnt lgkmcnt(0)
	global_store_dwordx4 v[244:245], v[246:249], off offset:256
	v_pk_mul_f32 v[16:17], v[92:93], s[18:19] op_sel_hi:[1,0]
	v_pk_mul_f32 v[18:19], v[90:91], s[18:19] op_sel_hi:[1,0]
	v_pk_mul_f32 v[10:11], v[100:101], s[18:19] op_sel_hi:[1,0]
	v_pk_mul_f32 v[12:13], v[98:99], s[18:19] op_sel_hi:[1,0]
	v_pk_mul_f32 v[20:21], v[2:3], v[10:11] op_sel_hi:[0,1]
	v_pk_mul_f32 v[10:11], v[2:3], v[12:13] op_sel_hi:[0,1]
	v_pk_mul_f32 v[16:17], v[2:3], v[16:17] op_sel_hi:[0,1]
	v_pk_mul_f32 v[12:13], v[2:3], v[18:19] op_sel_hi:[0,1]
	v_cvt_pk_bf16_f32 v10, v10, v11
	v_cvt_pk_bf16_f32 v11, v20, v21
	v_cvt_pk_bf16_f32 v12, v12, v13
	v_cvt_pk_bf16_f32 v13, v16, v17
	v_add_co_u32_e32 v16, vcc, s71, v4
	v_pk_mul_f32 v[18:19], v[78:79], s[18:19] op_sel_hi:[1,0]
	s_nop 0
	v_addc_co_u32_e32 v17, vcc, 0, v5, vcc
	ds_write_b128 v240, v[10:13]
	s_waitcnt lgkmcnt(0)
	s_barrier
	ds_read_b128 v[246:249], v241
	v_lshl_add_u64 v[244:245], v[16:17], 0, v[242:243]
	s_waitcnt lgkmcnt(0)
	global_store_dwordx4 v[244:245], v[246:249], off
	v_pk_mul_f32 v[16:17], v[80:81], s[18:19] op_sel_hi:[1,0]
	v_lshl_add_u64 v[14:15], v[4:5], 0, s[38:39]
	v_pk_mul_f32 v[10:11], v[88:89], s[18:19] op_sel_hi:[1,0]
	v_pk_mul_f32 v[12:13], v[86:87], s[18:19] op_sel_hi:[1,0]
	v_pk_mul_f32 v[20:21], v[2:3], v[10:11] op_sel_hi:[0,1]
	v_pk_mul_f32 v[10:11], v[2:3], v[12:13] op_sel_hi:[0,1]
	v_pk_mul_f32 v[12:13], v[2:3], v[18:19] op_sel_hi:[0,1]
	v_pk_mul_f32 v[16:17], v[2:3], v[16:17] op_sel_hi:[0,1]
	v_cvt_pk_bf16_f32 v10, v10, v11
	v_cvt_pk_bf16_f32 v11, v20, v21
	v_cvt_pk_bf16_f32 v12, v12, v13
	v_cvt_pk_bf16_f32 v13, v16, v17
	ds_write_b128 v240, v[10:13] offset:8192
	s_waitcnt lgkmcnt(0)
	s_barrier
	ds_read_b128 v[246:249], v241 offset:8192
	v_lshl_add_u64 v[244:245], v[14:15], 0, v[242:243]
	s_waitcnt lgkmcnt(0)
	global_store_dwordx4 v[244:245], v[246:249], off offset:256
	v_pk_mul_f32 v[18:19], v[74:75], s[18:19] op_sel_hi:[1,0]
	v_lshl_add_u64 v[14:15], v[4:5], 0, s[40:41]
	v_pk_mul_f32 v[10:11], v[84:85], s[18:19] op_sel_hi:[1,0]
	v_pk_mul_f32 v[12:13], v[82:83], s[18:19] op_sel_hi:[1,0]
	v_pk_mul_f32 v[16:17], v[76:77], s[18:19] op_sel_hi:[1,0]
	v_pk_mul_f32 v[20:21], v[2:3], v[10:11] op_sel_hi:[0,1]
	v_pk_mul_f32 v[10:11], v[2:3], v[12:13] op_sel_hi:[0,1]
	v_pk_mul_f32 v[12:13], v[2:3], v[18:19] op_sel_hi:[0,1]
	v_add_co_u32_e32 v4, vcc, s72, v4
	v_pk_mul_f32 v[16:17], v[2:3], v[16:17] op_sel_hi:[0,1]
	v_cvt_pk_bf16_f32 v10, v10, v11
	v_cvt_pk_bf16_f32 v11, v20, v21
	v_cvt_pk_bf16_f32 v12, v12, v13
	v_cvt_pk_bf16_f32 v13, v16, v17
	s_nop 0
	v_addc_co_u32_e32 v5, vcc, 0, v5, vcc
	ds_write_b128 v240, v[10:13]
	s_waitcnt lgkmcnt(0)
	s_barrier
	ds_read_b128 v[246:249], v241
	v_lshl_add_u64 v[244:245], v[4:5], 0, v[242:243]
	s_waitcnt lgkmcnt(0)
	global_store_dwordx4 v[244:245], v[246:249], off
	v_pk_mul_f32 v[16:17], v[66:67], s[18:19] op_sel_hi:[1,0]
	v_pk_mul_f32 v[4:5], v[72:73], s[18:19] op_sel_hi:[1,0]
	v_pk_mul_f32 v[10:11], v[70:71], s[18:19] op_sel_hi:[1,0]
	v_pk_mul_f32 v[12:13], v[68:69], s[18:19] op_sel_hi:[1,0]
	v_pk_mul_f32 v[10:11], v[2:3], v[10:11] op_sel_hi:[0,1]
	v_pk_mul_f32 v[18:19], v[2:3], v[12:13] op_sel_hi:[0,1]
	v_pk_mul_f32 v[12:13], v[2:3], v[16:17] op_sel_hi:[0,1]
	s_andn2_b64 vcc, exec, s[42:43]
	s_mov_b64 s[42:43], -1
	v_pk_mul_f32 v[4:5], v[2:3], v[4:5] op_sel_hi:[0,1]
	v_cvt_pk_bf16_f32 v10, v10, v11
	v_cvt_pk_bf16_f32 v11, v4, v5
	v_cvt_pk_bf16_f32 v12, v12, v13
	v_cvt_pk_bf16_f32 v13, v18, v19
	ds_write_b128 v240, v[10:13] offset:8192
	s_waitcnt lgkmcnt(0)
	s_barrier
	ds_read_b128 v[246:249], v241 offset:8192
	v_lshl_add_u64 v[244:245], v[14:15], 0, v[242:243]
	s_waitcnt lgkmcnt(0)
	s_barrier
	global_store_dwordx4 v[244:245], v[246:249], off offset:256
	s_cbranch_vccnz .LBB0_173
	s_andn2_b64 vcc, exec, s[14:15]
	s_cbranch_vccnz .LBB0_172
	s_barrier
	s_branch .LBB0_172

.LBB0_428:
	v_lshrrev_b32_e32 v3, 1, v196
	v_and_b32_e32 v3, 24, v3
	v_and_b32_e32 v2, 15, v196
	v_lshlrev_b32_e32 v8, 1, v3
	s_add_u32 s16, s16, 0x35f00000
	v_lshl_or_b32 v199, s19, 6, v2
	v_lshl_or_b32 v2, v2, 6, v8
	v_lshlrev_b32_e32 v8, 2, v196
	s_addc_u32 s17, s17, 0
	s_lshl_b32 s19, s19, 13
	v_and_b32_e32 v8, 32, v8
	v_bitop3_b32 v9, v2, s19, v8 bitop3:0xde
	s_lshl_b32 s19, s38, 5
	s_and_b32 s40, s19, 0x60
	s_lshl_b32 s19, s40, 7
	s_add_u32 s38, s12, 0x80
	v_bitop3_b32 v2, v2, s19, v8 bitop3:0xde
	s_waitcnt vmcnt(2)
	s_barrier
	s_addc_u32 s39, s13, 0
	s_add_i32 s61, s57, 0x18000
	s_mov_b32 s19, m0
	s_mov_b32 m0, s61
	s_nop 0
	global_load_lds_dwordx4 v197, s[38:39]
	s_mov_b32 m0, s19
	s_add_i32 s62, s57, 0x1a000
	s_mov_b32 s19, m0
	s_mov_b32 m0, s62
	s_nop 0
	global_load_lds_dwordx4 v198, s[38:39]
	s_mov_b32 m0, s19
	s_add_u32 s38, s10, 0x80
	s_addc_u32 s39, s11, 0
	s_add_i32 s63, s57, 0x8000
	s_mov_b32 s19, m0
	s_mov_b32 m0, s63
	s_nop 0
	global_load_lds_dwordx4 v218, s[38:39]
	s_mov_b32 m0, s19
	s_add_i32 s64, s57, 0xa000
	s_mov_b32 s19, m0
	s_mov_b32 m0, s64
	s_nop 0
	global_load_lds_dwordx4 v220, s[38:39]
	s_mov_b32 m0, s19
	s_add_u32 s38, s12, 0x20080
	s_addc_u32 s39, s13, 0
	s_add_i32 s65, s57, 0x1c000
	s_mov_b32 s19, m0
	s_mov_b32 m0, s65
	s_nop 0
	global_load_lds_dwordx4 v197, s[38:39]
	s_mov_b32 m0, s19
	s_add_i32 s66, s57, 0x1e000
	s_mov_b32 s19, m0
	s_mov_b32 m0, s66
	s_nop 0
	global_load_lds_dwordx4 v198, s[38:39]
	s_mov_b32 m0, s19
	s_waitcnt vmcnt(6)
	s_add_i32 s38, s57, 0xc000
	s_cmpk_lt_u32 s18, 0x100
	v_add_u32_e32 v201, 0, v2
	s_cselect_b64 s[18:19], -1, 0
	v_or_b32_e32 v200, s40, v3
	v_add_u32_e32 v202, 0x10000, v201
	v_add_u32_e32 v203, 0x14000, v201
	v_add_u32_e32 v204, 0, v9
	v_mov_b32_e32 v205, s38
	v_mov_b32_e32 v206, s57
	v_mov_b32_e32 v207, s9
	v_mov_b32_e32 v209, s20
	v_mov_b32_e32 v210, s28
	v_mov_b32_e32 v211, s29
	s_movk_i32 s67, 0x42
	s_mov_b32 s20, 0x3b800000
	s_mov_b64 s[28:29], 0x40000
	s_mov_b32 s68, 0x40000
	s_mov_b64 s[38:39], 0x48000
	s_mov_b32 s69, 0x48000
	s_mov_b64 s[40:41], 0x50000
	s_mov_b32 s70, 0x50000
	s_mov_b64 s[42:43], 0x58000
	s_mov_b32 s71, 0x58000
	v_mov_b64_e32 v[194:195], 0x207
	v_mov_b32_e32 v212, 1
	s_barrier
	s_waitcnt vmcnt(0)
	v_and_b32_e32 v250, 63, v0
	v_and_b32_e32 v251, 15, v250
	v_lshrrev_b32_e32 v252, 4, v250
	v_readfirstlane_b32 s99, v0
	s_lshr_b32 s99, s99, 6
	s_and_b32 s100, s99, 3
	s_lshr_b32 s101, s99, 2
	s_lshl_b32 s100, s100, 2
	v_add_u32_e32 v253, s100, v252
	v_xor_b32_e32 v254, v253, v251
	s_lshl_b32 s101, s101, 12
	s_add_i32 s101, s101, 0xc000
	v_lshlrev_b32_e32 v240, 8, v251
	v_lshl_add_u32 v240, v254, 4, v240
	v_add_u32_e32 v240, s101, v240
	v_lshlrev_b32_e32 v241, 8, v253
	v_lshl_add_u32 v241, v254, 4, v241
	v_add_u32_e32 v241, s101, v241
	v_sub_u32_e32 v242, v253, v251
	v_lshlrev_b32_e32 v242, 11, v242
	v_lshl_add_u32 v242, v251, 4, v242
	v_lshlrev_b32_e32 v244, 4, v253
	v_sub_u32_e32 v242, v242, v244
	v_ashrrev_i32_e32 v243, 31, v242
	s_branch .LBB0_431

.LBB0_452:
	v_lshl_add_u32 v12, s72, 8, v199
	v_lshl_or_b32 v2, s73, 8, v200
	v_ashrrev_i32_e32 v13, 31, v12
	v_ashrrev_i32_e32 v3, 31, v2
	v_lshlrev_b64 v[8:9], 11, v[12:13]
	v_lshl_add_u64 v[8:9], s[16:17], 0, v[8:9]
	v_lshlrev_b64 v[14:15], 1, v[2:3]
	v_lshl_add_u64 v[2:3], v[8:9], 0, v[14:15]
	v_pk_fma_f32 v[8:9], v[190:191], s[20:21], 0 op_sel_hi:[1,0,0]
	v_pk_fma_f32 v[10:11], v[192:193], s[20:21], 0 op_sel_hi:[1,0,0]
	v_cvt_pk_bf16_f32 v8, v8, v9
	v_pk_fma_f32 v[16:17], v[188:189], s[20:21], 0 op_sel_hi:[1,0,0]
	v_cvt_pk_bf16_f32 v9, v10, v11
	v_pk_fma_f32 v[18:19], v[186:187], s[20:21], 0 op_sel_hi:[1,0,0]
	v_pk_fma_f32 v[20:21], v[170:171], s[20:21], 0 op_sel_hi:[1,0,0]
	v_cvt_pk_bf16_f32 v10, v18, v19
	v_cvt_pk_bf16_f32 v11, v16, v17
	ds_write_b128 v240, v[8:11]
	s_waitcnt lgkmcnt(0)
	s_barrier
	ds_read_b128 v[246:249], v241
	v_lshl_add_u64 v[244:245], v[2:3], 0, v[242:243]
	s_waitcnt lgkmcnt(0)
	global_store_dwordx4 v[244:245], v[246:249], off
	v_pk_fma_f32 v[16:17], v[176:177], s[20:21], 0 op_sel_hi:[1,0,0]
	v_pk_fma_f32 v[18:19], v[174:175], s[20:21], 0 op_sel_hi:[1,0,0]
	v_pk_fma_f32 v[8:9], v[182:183], s[20:21], 0 op_sel_hi:[1,0,0]
	v_pk_fma_f32 v[10:11], v[184:185], s[20:21], 0 op_sel_hi:[1,0,0]
	v_cvt_pk_bf16_f32 v8, v8, v9
	s_nop 0
	v_cvt_pk_bf16_f32 v9, v10, v11
	v_cvt_pk_bf16_f32 v10, v18, v19
	v_cvt_pk_bf16_f32 v11, v16, v17
	ds_write_b128 v240, v[8:11] offset:8192
	s_waitcnt lgkmcnt(0)
	s_barrier
	ds_read_b128 v[246:249], v241 offset:8192
	v_lshl_add_u64 v[244:245], v[2:3], 0, v[242:243]
	s_waitcnt lgkmcnt(0)
	global_store_dwordx4 v[244:245], v[246:249], off offset:256
	v_pk_fma_f32 v[18:19], v[172:173], s[20:21], 0 op_sel_hi:[1,0,0]
	s_nop 0
	v_or_b32_e32 v8, 16, v12
	v_ashrrev_i32_e32 v9, 31, v8
	v_lshlrev_b64 v[8:9], 11, v[8:9]
	v_lshl_add_u64 v[8:9], s[16:17], 0, v[8:9]
	v_lshl_add_u64 v[16:17], v[8:9], 0, v[14:15]
	v_pk_fma_f32 v[8:9], v[178:179], s[20:21], 0 op_sel_hi:[1,0,0]
	v_pk_fma_f32 v[10:11], v[180:181], s[20:21], 0 op_sel_hi:[1,0,0]
	v_cvt_pk_bf16_f32 v8, v8, v9
	s_nop 0
	v_cvt_pk_bf16_f32 v9, v10, v11
	v_cvt_pk_bf16_f32 v10, v20, v21
	v_cvt_pk_bf16_f32 v11, v18, v19
	ds_write_b128 v240, v[8:11]
	s_waitcnt lgkmcnt(0)
	s_barrier
	ds_read_b128 v[246:249], v241
	v_lshl_add_u64 v[244:245], v[16:17], 0, v[242:243]
	s_waitcnt lgkmcnt(0)
	global_store_dwordx4 v[244:245], v[246:249], off
	v_pk_fma_f32 v[18:19], v[160:161], s[20:21], 0 op_sel_hi:[1,0,0]
	v_pk_fma_f32 v[20:21], v[158:159], s[20:21], 0 op_sel_hi:[1,0,0]
	v_pk_fma_f32 v[8:9], v[166:167], s[20:21], 0 op_sel_hi:[1,0,0]
	v_pk_fma_f32 v[10:11], v[168:169], s[20:21], 0 op_sel_hi:[1,0,0]
	v_cvt_pk_bf16_f32 v8, v8, v9
	s_nop 0
	v_cvt_pk_bf16_f32 v9, v10, v11
	v_cvt_pk_bf16_f32 v10, v20, v21
	v_cvt_pk_bf16_f32 v11, v18, v19
	ds_write_b128 v240, v[8:11] offset:8192
	s_waitcnt lgkmcnt(0)
	s_barrier
	ds_read_b128 v[246:249], v241 offset:8192
	v_lshl_add_u64 v[244:245], v[16:17], 0, v[242:243]
	s_waitcnt lgkmcnt(0)
	global_store_dwordx4 v[244:245], v[246:249], off offset:256
	v_pk_fma_f32 v[18:19], v[156:157], s[20:21], 0 op_sel_hi:[1,0,0]
	v_pk_fma_f32 v[20:21], v[154:155], s[20:21], 0 op_sel_hi:[1,0,0]
	v_or_b32_e32 v8, 32, v12
	v_ashrrev_i32_e32 v9, 31, v8
	v_lshlrev_b64 v[8:9], 11, v[8:9]
	v_lshl_add_u64 v[8:9], s[16:17], 0, v[8:9]
	v_lshl_add_u64 v[16:17], v[8:9], 0, v[14:15]
	v_pk_fma_f32 v[8:9], v[162:163], s[20:21], 0 op_sel_hi:[1,0,0]
	v_pk_fma_f32 v[10:11], v[164:165], s[20:21], 0 op_sel_hi:[1,0,0]
	v_cvt_pk_bf16_f32 v8, v8, v9
	s_nop 0
	v_cvt_pk_bf16_f32 v9, v10, v11
	v_cvt_pk_bf16_f32 v10, v20, v21
	v_cvt_pk_bf16_f32 v11, v18, v19
	ds_write_b128 v240, v[8:11]
	s_waitcnt lgkmcnt(0)
	s_barrier
	ds_read_b128 v[246:249], v241
	v_lshl_add_u64 v[244:245], v[16:17], 0, v[242:243]
	s_waitcnt lgkmcnt(0)
	global_store_dwordx4 v[244:245], v[246:249], off
	v_pk_fma_f32 v[18:19], v[144:145], s[20:21], 0 op_sel_hi:[1,0,0]
	v_pk_fma_f32 v[20:21], v[142:143], s[20:21], 0 op_sel_hi:[1,0,0]
	v_pk_fma_f32 v[8:9], v[150:151], s[20:21], 0 op_sel_hi:[1,0,0]
	v_pk_fma_f32 v[10:11], v[152:153], s[20:21], 0 op_sel_hi:[1,0,0]
	v_cvt_pk_bf16_f32 v8, v8, v9
	s_nop 0
	v_cvt_pk_bf16_f32 v9, v10, v11
	v_cvt_pk_bf16_f32 v10, v20, v21
	v_cvt_pk_bf16_f32 v11, v18, v19
	ds_write_b128 v240, v[8:11] offset:8192
	s_waitcnt lgkmcnt(0)
	s_barrier
	ds_read_b128 v[246:249], v241 offset:8192
	v_lshl_add_u64 v[244:245], v[16:17], 0, v[242:243]
	s_waitcnt lgkmcnt(0)
	global_store_dwordx4 v[244:245], v[246:249], off offset:256
	v_pk_fma_f32 v[16:17], v[138:139], s[20:21], 0 op_sel_hi:[1,0,0]
	s_nop 0
	v_or_b32_e32 v8, 48, v12
	v_ashrrev_i32_e32 v9, 31, v8
	v_lshlrev_b64 v[8:9], 11, v[8:9]
	v_lshl_add_u64 v[8:9], s[16:17], 0, v[8:9]
	v_lshl_add_u64 v[12:13], v[8:9], 0, v[14:15]
	v_pk_fma_f32 v[10:11], v[148:149], s[20:21], 0 op_sel_hi:[1,0,0]
	v_pk_fma_f32 v[8:9], v[146:147], s[20:21], 0 op_sel_hi:[1,0,0]
	v_pk_fma_f32 v[14:15], v[140:141], s[20:21], 0 op_sel_hi:[1,0,0]
	v_cvt_pk_bf16_f32 v8, v8, v9
	v_cvt_pk_bf16_f32 v9, v10, v11
	v_cvt_pk_bf16_f32 v10, v16, v17
	v_pk_fma_f32 v[16:17], v[130:131], s[20:21], 0 op_sel_hi:[1,0,0]
	v_cvt_pk_bf16_f32 v11, v14, v15
	ds_write_b128 v240, v[8:11]
	s_waitcnt lgkmcnt(0)
	s_barrier
	ds_read_b128 v[246:249], v241
	v_lshl_add_u64 v[244:245], v[12:13], 0, v[242:243]
	s_waitcnt lgkmcnt(0)
	global_store_dwordx4 v[244:245], v[246:249], off
	v_pk_fma_f32 v[14:15], v[132:133], s[20:21], 0 op_sel_hi:[1,0,0]
	s_nop 0
	v_pk_fma_f32 v[10:11], v[136:137], s[20:21], 0 op_sel_hi:[1,0,0]
	v_pk_fma_f32 v[8:9], v[134:135], s[20:21], 0 op_sel_hi:[1,0,0]
	s_nop 0
	v_cvt_pk_bf16_f32 v8, v8, v9
	v_cvt_pk_bf16_f32 v9, v10, v11
	v_cvt_pk_bf16_f32 v10, v16, v17
	v_cvt_pk_bf16_f32 v11, v14, v15
	ds_write_b128 v240, v[8:11] offset:8192
	s_waitcnt lgkmcnt(0)
	s_barrier
	ds_read_b128 v[246:249], v241 offset:8192
	v_lshl_add_u64 v[244:245], v[12:13], 0, v[242:243]
	s_waitcnt lgkmcnt(0)
	global_store_dwordx4 v[244:245], v[246:249], off offset:256
	v_pk_fma_f32 v[14:15], v[124:125], s[20:21], 0 op_sel_hi:[1,0,0]
	v_pk_fma_f32 v[16:17], v[122:123], s[20:21], 0 op_sel_hi:[1,0,0]
	v_pk_fma_f32 v[10:11], v[128:129], s[20:21], 0 op_sel_hi:[1,0,0]
	v_pk_fma_f32 v[8:9], v[126:127], s[20:21], 0 op_sel_hi:[1,0,0]
	v_lshl_add_u64 v[12:13], v[2:3], 0, s[28:29]
	v_cvt_pk_bf16_f32 v8, v8, v9
	v_cvt_pk_bf16_f32 v9, v10, v11
	v_cvt_pk_bf16_f32 v10, v16, v17
	v_cvt_pk_bf16_f32 v11, v14, v15
	v_add_co_u32_e32 v14, vcc, s68, v2
	v_pk_fma_f32 v[16:17], v[110:111], s[20:21], 0 op_sel_hi:[1,0,0]
	s_nop 0
	v_addc_co_u32_e32 v15, vcc, 0, v3, vcc
	ds_write_b128 v240, v[8:11]
	s_waitcnt lgkmcnt(0)
	s_barrier
	ds_read_b128 v[246:249], v241
	v_lshl_add_u64 v[244:245], v[14:15], 0, v[242:243]
	s_waitcnt lgkmcnt(0)
	global_store_dwordx4 v[244:245], v[246:249], off
	v_pk_fma_f32 v[14:15], v[112:113], s[20:21], 0 op_sel_hi:[1,0,0]
	s_nop 0
	v_pk_fma_f32 v[10:11], v[120:121], s[20:21], 0 op_sel_hi:[1,0,0]
	v_pk_fma_f32 v[8:9], v[118:119], s[20:21], 0 op_sel_hi:[1,0,0]
	s_nop 0
	v_cvt_pk_bf16_f32 v8, v8, v9
	v_cvt_pk_bf16_f32 v9, v10, v11
	v_cvt_pk_bf16_f32 v10, v16, v17
	v_cvt_pk_bf16_f32 v11, v14, v15
	ds_write_b128 v240, v[8:11] offset:8192
	s_waitcnt lgkmcnt(0)
	s_barrier
	ds_read_b128 v[246:249], v241 offset:8192
	v_lshl_add_u64 v[244:245], v[12:13], 0, v[242:243]
	s_waitcnt lgkmcnt(0)
	global_store_dwordx4 v[244:245], v[246:249], off offset:256
	v_pk_fma_f32 v[14:15], v[108:109], s[20:21], 0 op_sel_hi:[1,0,0]
	v_pk_fma_f32 v[16:17], v[106:107], s[20:21], 0 op_sel_hi:[1,0,0]
	v_pk_fma_f32 v[10:11], v[116:117], s[20:21], 0 op_sel_hi:[1,0,0]
	v_pk_fma_f32 v[8:9], v[114:115], s[20:21], 0 op_sel_hi:[1,0,0]
	v_lshl_add_u64 v[12:13], v[2:3], 0, s[38:39]
	v_cvt_pk_bf16_f32 v8, v8, v9
	v_cvt_pk_bf16_f32 v9, v10, v11
	v_cvt_pk_bf16_f32 v10, v16, v17
	v_cvt_pk_bf16_f32 v11, v14, v15
	v_add_co_u32_e32 v14, vcc, s69, v2
	v_pk_fma_f32 v[16:17], v[94:95], s[20:21], 0 op_sel_hi:[1,0,0]
	s_nop 0
	v_addc_co_u32_e32 v15, vcc, 0, v3, vcc
	ds_write_b128 v240, v[8:11]
	s_waitcnt lgkmcnt(0)
	s_barrier
	ds_read_b128 v[246:249], v241
	v_lshl_add_u64 v[244:245], v[14:15], 0, v[242:243]
	s_waitcnt lgkmcnt(0)
	global_store_dwordx4 v[244:245], v[246:249], off
	v_pk_fma_f32 v[14:15], v[96:97], s[20:21], 0 op_sel_hi:[1,0,0]
	s_nop 0
	v_pk_fma_f32 v[10:11], v[104:105], s[20:21], 0 op_sel_hi:[1,0,0]
	v_pk_fma_f32 v[8:9], v[102:103], s[20:21], 0 op_sel_hi:[1,0,0]
	s_nop 0
	v_cvt_pk_bf16_f32 v8, v8, v9
	v_cvt_pk_bf16_f32 v9, v10, v11
	v_cvt_pk_bf16_f32 v10, v16, v17
	v_cvt_pk_bf16_f32 v11, v14, v15
	ds_write_b128 v240, v[8:11] offset:8192
	s_waitcnt lgkmcnt(0)
	s_barrier
	ds_read_b128 v[246:249], v241 offset:8192
	v_lshl_add_u64 v[244:245], v[12:13], 0, v[242:243]
	s_waitcnt lgkmcnt(0)
	global_store_dwordx4 v[244:245], v[246:249], off offset:256
	v_pk_fma_f32 v[14:15], v[92:93], s[20:21], 0 op_sel_hi:[1,0,0]
	v_pk_fma_f32 v[16:17], v[90:91], s[20:21], 0 op_sel_hi:[1,0,0]
	v_pk_fma_f32 v[10:11], v[100:101], s[20:21], 0 op_sel_hi:[1,0,0]
	v_pk_fma_f32 v[8:9], v[98:99], s[20:21], 0 op_sel_hi:[1,0,0]
	v_lshl_add_u64 v[12:13], v[2:3], 0, s[40:41]
	v_cvt_pk_bf16_f32 v8, v8, v9
	v_cvt_pk_bf16_f32 v9, v10, v11
	v_cvt_pk_bf16_f32 v10, v16, v17
	v_cvt_pk_bf16_f32 v11, v14, v15
	v_add_co_u32_e32 v14, vcc, s70, v2
	v_pk_fma_f32 v[16:17], v[78:79], s[20:21], 0 op_sel_hi:[1,0,0]
	s_nop 0
	v_addc_co_u32_e32 v15, vcc, 0, v3, vcc
	ds_write_b128 v240, v[8:11]
	s_waitcnt lgkmcnt(0)
	s_barrier
	ds_read_b128 v[246:249], v241
	v_lshl_add_u64 v[244:245], v[14:15], 0, v[242:243]
	s_waitcnt lgkmcnt(0)
	global_store_dwordx4 v[244:245], v[246:249], off
	v_pk_fma_f32 v[14:15], v[80:81], s[20:21], 0 op_sel_hi:[1,0,0]
	s_nop 0
	v_pk_fma_f32 v[10:11], v[88:89], s[20:21], 0 op_sel_hi:[1,0,0]
	v_pk_fma_f32 v[8:9], v[86:87], s[20:21], 0 op_sel_hi:[1,0,0]
	s_nop 0
	v_cvt_pk_bf16_f32 v8, v8, v9
	v_cvt_pk_bf16_f32 v9, v10, v11
	v_cvt_pk_bf16_f32 v10, v16, v17
	v_cvt_pk_bf16_f32 v11, v14, v15
	ds_write_b128 v240, v[8:11] offset:8192
	s_waitcnt lgkmcnt(0)
	s_barrier
	ds_read_b128 v[246:249], v241 offset:8192
	v_lshl_add_u64 v[244:245], v[12:13], 0, v[242:243]
	s_waitcnt lgkmcnt(0)
	global_store_dwordx4 v[244:245], v[246:249], off offset:256
	v_lshl_add_u64 v[12:13], v[2:3], 0, s[42:43]
	v_add_co_u32_e32 v2, vcc, s71, v2
	v_pk_fma_f32 v[10:11], v[84:85], s[20:21], 0 op_sel_hi:[1,0,0]
	v_pk_fma_f32 v[8:9], v[82:83], s[20:21], 0 op_sel_hi:[1,0,0]
	v_pk_fma_f32 v[14:15], v[76:77], s[20:21], 0 op_sel_hi:[1,0,0]
	v_pk_fma_f32 v[16:17], v[74:75], s[20:21], 0 op_sel_hi:[1,0,0]
	v_cvt_pk_bf16_f32 v8, v8, v9
	v_cvt_pk_bf16_f32 v9, v10, v11
	v_addc_co_u32_e32 v3, vcc, 0, v3, vcc
	v_cvt_pk_bf16_f32 v10, v16, v17
	v_cvt_pk_bf16_f32 v11, v14, v15
	ds_write_b128 v240, v[8:11]
	s_waitcnt lgkmcnt(0)
	s_barrier
	ds_read_b128 v[246:249], v241
	v_lshl_add_u64 v[244:245], v[2:3], 0, v[242:243]
	s_waitcnt lgkmcnt(0)
	global_store_dwordx4 v[244:245], v[246:249], off
	s_andn2_b64 vcc, exec, s[44:45]
	s_mov_b64 s[44:45], -1
	v_pk_fma_f32 v[8:9], v[70:71], s[20:21], 0 op_sel_hi:[1,0,0]
	v_pk_fma_f32 v[10:11], v[66:67], s[20:21], 0 op_sel_hi:[1,0,0]
	v_pk_fma_f32 v[2:3], v[72:73], s[20:21], 0 op_sel_hi:[1,0,0]
	v_pk_fma_f32 v[14:15], v[68:69], s[20:21], 0 op_sel_hi:[1,0,0]
	v_cvt_pk_bf16_f32 v8, v8, v9
	v_cvt_pk_bf16_f32 v9, v2, v3
	v_cvt_pk_bf16_f32 v10, v10, v11
	s_nop 0
	v_cvt_pk_bf16_f32 v11, v14, v15
	ds_write_b128 v240, v[8:11] offset:8192
	s_waitcnt lgkmcnt(0)
	s_barrier
	ds_read_b128 v[246:249], v241 offset:8192
	v_lshl_add_u64 v[244:245], v[12:13], 0, v[242:243]
	s_waitcnt lgkmcnt(0)
	s_barrier
	global_store_dwordx4 v[244:245], v[246:249], off offset:256
	s_cbranch_vccnz .LBB0_430
	s_andn2_b64 vcc, exec, s[14:15]
	s_cbranch_vccnz .LBB0_429
	s_barrier
	s_branch .LBB0_429

.LBB0_787:
	s_add_u32 s38, s4, 0x4b400000
	s_addc_u32 s39, s5, 0
	v_lshrrev_b32_e32 v3, 1, v194
	s_add_u32 s4, s18, 0x80
	v_and_b32_e32 v3, 24, v3
	s_addc_u32 s5, s19, 0
	v_and_b32_e32 v2, 15, v194
	v_lshlrev_b32_e32 v4, 1, v3
	s_cmp_lg_u64 s[16:17], 0
	v_lshl_or_b32 v197, s43, 6, v2
	v_lshl_or_b32 v2, v2, 6, v4
	v_lshlrev_b32_e32 v4, 2, v194
	s_cselect_b64 s[40:41], -1, 0
	s_lshl_b32 s43, s43, 13
	v_and_b32_e32 v4, 32, v4
	v_bitop3_b32 v5, v2, s43, v4 bitop3:0xde
	s_lshl_b32 s43, s47, 5
	s_and_b32 s47, s43, 0x60
	s_lshl_b32 s43, s47, 7
	s_add_u32 s48, s20, 0x80
	v_bitop3_b32 v2, v2, s43, v4 bitop3:0xde
	s_waitcnt vmcnt(2)
	s_barrier
	s_addc_u32 s49, s21, 0
	s_add_i32 s77, s73, 0x18000
	s_mov_b32 s43, m0
	s_mov_b32 m0, s77
	s_nop 0
	global_load_lds_dwordx4 v195, s[48:49]
	s_mov_b32 m0, s43
	s_add_i32 s78, s73, 0x1a000
	s_mov_b32 s43, m0
	s_mov_b32 m0, s78
	s_nop 0
	global_load_lds_dwordx4 v196, s[48:49]
	s_mov_b32 m0, s43
	s_add_i32 s79, s73, 0x8000
	s_mov_b32 s43, m0
	s_mov_b32 m0, s79
	s_nop 0
	global_load_lds_dwordx4 v216, s[4:5]
	s_mov_b32 m0, s43
	s_add_i32 s80, s73, 0xa000
	s_mov_b32 s43, m0
	s_mov_b32 m0, s80
	s_nop 0
	global_load_lds_dwordx4 v218, s[4:5]
	s_mov_b32 m0, s43
	s_add_u32 s4, s20, 0x20080
	s_addc_u32 s5, s21, 0
	s_add_i32 s81, s73, 0x1c000
	s_mov_b32 s43, m0
	s_mov_b32 m0, s81
	s_nop 0
	global_load_lds_dwordx4 v195, s[4:5]
	s_mov_b32 m0, s43
	s_add_i32 s82, s73, 0x1e000
	s_mov_b32 s43, m0
	s_mov_b32 m0, s82
	s_nop 0
	global_load_lds_dwordx4 v196, s[4:5]
	s_mov_b32 m0, s43
	s_waitcnt vmcnt(6)
	s_add_i32 s4, s73, 0xc000
	s_cmpk_lt_u32 s42, 0x100
	v_add_u32_e32 v199, 0, v2
	s_cselect_b64 s[42:43], -1, 0
	v_or_b32_e32 v198, s47, v3
	v_add_u32_e32 v200, 0x10000, v199
	v_add_u32_e32 v201, 0x14000, v199
	v_add_u32_e32 v202, 0, v5
	v_mov_b32_e32 v203, s4
	v_mov_b32_e32 v204, s73
	v_mov_b32_e32 v205, s13
	v_mov_b32_e32 v206, s15
	v_mov_b32_e32 v207, s44
	v_mov_b32_e32 v209, s46
	s_mov_b32 s44, 0x3d000000
	s_mov_b32 s83, 0x40000
	s_mov_b64 s[46:47], 0x48000
	s_mov_b32 s84, 0x48000
	s_mov_b64 s[48:49], 0x50000
	s_mov_b32 s85, 0x50000
	s_mov_b64 s[50:51], 0x58000
	s_mov_b32 s86, 0x58000
	v_mov_b32_e32 v210, 1
	s_barrier
	v_and_b32_e32 v250, 63, v0
	v_and_b32_e32 v251, 15, v250
	v_lshrrev_b32_e32 v252, 4, v250
	v_readfirstlane_b32 s99, v0
	s_lshr_b32 s99, s99, 6
	s_and_b32 s100, s99, 3
	s_lshr_b32 s101, s99, 2
	s_lshl_b32 s100, s100, 2
	v_add_u32_e32 v253, s100, v252
	v_xor_b32_e32 v254, v253, v251
	s_lshl_b32 s101, s101, 12
	s_add_i32 s101, s101, 0xc000
	v_lshlrev_b32_e32 v240, 8, v251
	v_lshl_add_u32 v240, v254, 4, v240
	v_add_u32_e32 v240, s101, v240
	v_lshlrev_b32_e32 v241, 8, v253
	v_lshl_add_u32 v241, v254, 4, v241
	v_add_u32_e32 v241, s101, v241
	v_sub_u32_e32 v242, v253, v251
	v_lshlrev_b32_e32 v242, 11, v242
	v_lshl_add_u32 v242, v251, 4, v242
	v_lshlrev_b32_e32 v244, 4, v253
	v_sub_u32_e32 v242, v242, v244
	v_ashrrev_i32_e32 v243, 31, v242
	s_branch .LBB0_790

.LBB0_823:
	v_lshl_add_u32 v20, s87, 8, v197
	v_ashrrev_i32_e32 v21, 31, v20
	v_lshlrev_b64 v[26:27], 11, v[20:21]
	v_lshl_add_u64 v[26:27], s[38:39], 0, v[26:27]
	v_lshlrev_b64 v[30:31], 1, v[18:19]
	v_lshl_add_u64 v[18:19], v[26:27], 0, v[30:31]
	s_waitcnt vmcnt(0)
	v_pk_fma_f32 v[26:27], v[190:191], s[44:45], v[6:7] op_sel_hi:[1,0,1]
	v_pk_fma_f32 v[28:29], v[192:193], s[44:45], v[8:9] op_sel_hi:[1,0,1]
	v_cvt_pk_bf16_f32 v26, v26, v27
	v_pk_fma_f32 v[32:33], v[188:189], s[44:45], v[4:5] op_sel_hi:[1,0,1]
	v_cvt_pk_bf16_f32 v27, v28, v29
	v_pk_fma_f32 v[34:35], v[186:187], s[44:45], v[2:3] op_sel_hi:[1,0,1]
	v_pk_fma_f32 v[36:37], v[170:171], s[44:45], v[2:3] op_sel_hi:[1,0,1]
	v_cvt_pk_bf16_f32 v28, v34, v35
	v_cvt_pk_bf16_f32 v29, v32, v33
	ds_write_b128 v240, v[26:29]
	s_waitcnt lgkmcnt(0)
	s_barrier
	ds_read_b128 v[246:249], v241
	v_lshl_add_u64 v[244:245], v[18:19], 0, v[242:243]
	s_waitcnt lgkmcnt(0)
	global_store_dwordx4 v[244:245], v[246:249], off
	v_pk_fma_f32 v[32:33], v[176:177], s[44:45], v[12:13] op_sel_hi:[1,0,1]
	v_pk_fma_f32 v[34:35], v[174:175], s[44:45], v[10:11] op_sel_hi:[1,0,1]
	v_pk_fma_f32 v[26:27], v[182:183], s[44:45], v[14:15] op_sel_hi:[1,0,1]
	v_pk_fma_f32 v[28:29], v[184:185], s[44:45], v[16:17] op_sel_hi:[1,0,1]
	v_cvt_pk_bf16_f32 v26, v26, v27
	s_mov_b64 s[4:5], 0x40000
	v_cvt_pk_bf16_f32 v27, v28, v29
	v_cvt_pk_bf16_f32 v28, v34, v35
	v_cvt_pk_bf16_f32 v29, v32, v33
	ds_write_b128 v240, v[26:29] offset:8192
	s_waitcnt lgkmcnt(0)
	s_barrier
	ds_read_b128 v[246:249], v241 offset:8192
	v_lshl_add_u64 v[244:245], v[18:19], 0, v[242:243]
	s_waitcnt lgkmcnt(0)
	global_store_dwordx4 v[244:245], v[246:249], off offset:256
	v_pk_fma_f32 v[34:35], v[172:173], s[44:45], v[4:5] op_sel_hi:[1,0,1]
	s_nop 0
	v_or_b32_e32 v26, 16, v20
	v_ashrrev_i32_e32 v27, 31, v26
	v_lshlrev_b64 v[26:27], 11, v[26:27]
	v_lshl_add_u64 v[26:27], s[38:39], 0, v[26:27]
	v_lshl_add_u64 v[32:33], v[26:27], 0, v[30:31]
	v_pk_fma_f32 v[26:27], v[178:179], s[44:45], v[6:7] op_sel_hi:[1,0,1]
	v_pk_fma_f32 v[28:29], v[180:181], s[44:45], v[8:9] op_sel_hi:[1,0,1]
	v_cvt_pk_bf16_f32 v26, v26, v27
	s_nop 0
	v_cvt_pk_bf16_f32 v27, v28, v29
	v_cvt_pk_bf16_f32 v28, v36, v37
	v_cvt_pk_bf16_f32 v29, v34, v35
	ds_write_b128 v240, v[26:29]
	s_waitcnt lgkmcnt(0)
	s_barrier
	ds_read_b128 v[246:249], v241
	v_lshl_add_u64 v[244:245], v[32:33], 0, v[242:243]
	s_waitcnt lgkmcnt(0)
	global_store_dwordx4 v[244:245], v[246:249], off
	v_pk_fma_f32 v[34:35], v[160:161], s[44:45], v[12:13] op_sel_hi:[1,0,1]
	v_pk_fma_f32 v[36:37], v[158:159], s[44:45], v[10:11] op_sel_hi:[1,0,1]
	v_pk_fma_f32 v[26:27], v[166:167], s[44:45], v[14:15] op_sel_hi:[1,0,1]
	v_pk_fma_f32 v[28:29], v[168:169], s[44:45], v[16:17] op_sel_hi:[1,0,1]
	v_cvt_pk_bf16_f32 v26, v26, v27
	s_nop 0
	v_cvt_pk_bf16_f32 v27, v28, v29
	v_cvt_pk_bf16_f32 v28, v36, v37
	v_cvt_pk_bf16_f32 v29, v34, v35
	ds_write_b128 v240, v[26:29] offset:8192
	s_waitcnt lgkmcnt(0)
	s_barrier
	ds_read_b128 v[246:249], v241 offset:8192
	v_lshl_add_u64 v[244:245], v[32:33], 0, v[242:243]
	s_waitcnt lgkmcnt(0)
	global_store_dwordx4 v[244:245], v[246:249], off offset:256
	v_pk_fma_f32 v[34:35], v[156:157], s[44:45], v[4:5] op_sel_hi:[1,0,1]
	v_pk_fma_f32 v[36:37], v[154:155], s[44:45], v[2:3] op_sel_hi:[1,0,1]
	v_or_b32_e32 v26, 32, v20
	v_ashrrev_i32_e32 v27, 31, v26
	v_lshlrev_b64 v[26:27], 11, v[26:27]
	v_lshl_add_u64 v[26:27], s[38:39], 0, v[26:27]
	v_lshl_add_u64 v[32:33], v[26:27], 0, v[30:31]
	v_pk_fma_f32 v[28:29], v[164:165], s[44:45], v[8:9] op_sel_hi:[1,0,1]
	v_pk_fma_f32 v[26:27], v[162:163], s[44:45], v[6:7] op_sel_hi:[1,0,1]
	v_or_b32_e32 v20, 48, v20
	v_cvt_pk_bf16_f32 v26, v26, v27
	v_cvt_pk_bf16_f32 v27, v28, v29
	v_cvt_pk_bf16_f32 v28, v36, v37
	v_cvt_pk_bf16_f32 v29, v34, v35
	ds_write_b128 v240, v[26:29]
	s_waitcnt lgkmcnt(0)
	s_barrier
	ds_read_b128 v[246:249], v241
	v_lshl_add_u64 v[244:245], v[32:33], 0, v[242:243]
	s_waitcnt lgkmcnt(0)
	global_store_dwordx4 v[244:245], v[246:249], off
	v_ashrrev_i32_e32 v21, 31, v20
	v_pk_fma_f32 v[34:35], v[144:145], s[44:45], v[12:13] op_sel_hi:[1,0,1]
	v_pk_fma_f32 v[28:29], v[152:153], s[44:45], v[16:17] op_sel_hi:[1,0,1]
	v_pk_fma_f32 v[26:27], v[150:151], s[44:45], v[14:15] op_sel_hi:[1,0,1]
	v_pk_fma_f32 v[36:37], v[142:143], s[44:45], v[10:11] op_sel_hi:[1,0,1]
	v_cvt_pk_bf16_f32 v26, v26, v27
	v_cvt_pk_bf16_f32 v27, v28, v29
	v_lshlrev_b64 v[20:21], 11, v[20:21]
	v_cvt_pk_bf16_f32 v28, v36, v37
	v_cvt_pk_bf16_f32 v29, v34, v35
	ds_write_b128 v240, v[26:29] offset:8192
	s_waitcnt lgkmcnt(0)
	s_barrier
	ds_read_b128 v[246:249], v241 offset:8192
	v_lshl_add_u64 v[244:245], v[32:33], 0, v[242:243]
	s_waitcnt lgkmcnt(0)
	global_store_dwordx4 v[244:245], v[246:249], off offset:256
	v_lshl_add_u64 v[20:21], s[38:39], 0, v[20:21]
	v_lshl_add_u64 v[20:21], v[20:21], 0, v[30:31]
	v_pk_fma_f32 v[28:29], v[148:149], s[44:45], v[8:9] op_sel_hi:[1,0,1]
	v_pk_fma_f32 v[26:27], v[146:147], s[44:45], v[6:7] op_sel_hi:[1,0,1]
	v_pk_fma_f32 v[30:31], v[140:141], s[44:45], v[4:5] op_sel_hi:[1,0,1]
	v_pk_fma_f32 v[32:33], v[138:139], s[44:45], v[2:3] op_sel_hi:[1,0,1]
	v_cvt_pk_bf16_f32 v26, v26, v27
	v_cvt_pk_bf16_f32 v27, v28, v29
	s_nop 0
	v_cvt_pk_bf16_f32 v28, v32, v33
	v_cvt_pk_bf16_f32 v29, v30, v31
	ds_write_b128 v240, v[26:29]
	s_waitcnt lgkmcnt(0)
	s_barrier
	ds_read_b128 v[246:249], v241
	v_lshl_add_u64 v[244:245], v[20:21], 0, v[242:243]
	s_waitcnt lgkmcnt(0)
	global_store_dwordx4 v[244:245], v[246:249], off
	v_pk_fma_f32 v[30:31], v[132:133], s[44:45], v[12:13] op_sel_hi:[1,0,1]
	v_pk_fma_f32 v[32:33], v[130:131], s[44:45], v[10:11] op_sel_hi:[1,0,1]
	v_pk_fma_f32 v[28:29], v[136:137], s[44:45], v[16:17] op_sel_hi:[1,0,1]
	v_pk_fma_f32 v[26:27], v[134:135], s[44:45], v[14:15] op_sel_hi:[1,0,1]
	s_nop 0
	v_cvt_pk_bf16_f32 v26, v26, v27
	v_cvt_pk_bf16_f32 v27, v28, v29
	v_cvt_pk_bf16_f32 v28, v32, v33
	v_cvt_pk_bf16_f32 v29, v30, v31
	ds_write_b128 v240, v[26:29] offset:8192
	s_waitcnt lgkmcnt(0)
	s_barrier
	ds_read_b128 v[246:249], v241 offset:8192
	v_lshl_add_u64 v[244:245], v[20:21], 0, v[242:243]
	s_waitcnt lgkmcnt(0)
	global_store_dwordx4 v[244:245], v[246:249], off offset:256
	v_pk_fma_f32 v[30:31], v[124:125], s[44:45], v[4:5] op_sel_hi:[1,0,1]
	v_pk_fma_f32 v[32:33], v[122:123], s[44:45], v[2:3] op_sel_hi:[1,0,1]
	v_pk_fma_f32 v[28:29], v[128:129], s[44:45], v[8:9] op_sel_hi:[1,0,1]
	v_pk_fma_f32 v[26:27], v[126:127], s[44:45], v[6:7] op_sel_hi:[1,0,1]
	v_lshl_add_u64 v[20:21], v[18:19], 0, s[4:5]
	v_cvt_pk_bf16_f32 v26, v26, v27
	v_cvt_pk_bf16_f32 v27, v28, v29
	v_cvt_pk_bf16_f32 v28, v32, v33
	v_cvt_pk_bf16_f32 v29, v30, v31
	v_add_co_u32_e32 v30, vcc, s83, v18
	v_pk_fma_f32 v[32:33], v[110:111], s[44:45], v[10:11] op_sel_hi:[1,0,1]
	s_nop 0
	v_addc_co_u32_e32 v31, vcc, 0, v19, vcc
	ds_write_b128 v240, v[26:29]
	s_waitcnt lgkmcnt(0)
	s_barrier
	ds_read_b128 v[246:249], v241
	v_lshl_add_u64 v[244:245], v[30:31], 0, v[242:243]
	s_waitcnt lgkmcnt(0)
	global_store_dwordx4 v[244:245], v[246:249], off
	v_pk_fma_f32 v[30:31], v[112:113], s[44:45], v[12:13] op_sel_hi:[1,0,1]
	s_mov_b64 s[4:5], -1
	v_pk_fma_f32 v[28:29], v[120:121], s[44:45], v[16:17] op_sel_hi:[1,0,1]
	v_pk_fma_f32 v[26:27], v[118:119], s[44:45], v[14:15] op_sel_hi:[1,0,1]
	s_nop 0
	v_cvt_pk_bf16_f32 v26, v26, v27
	v_cvt_pk_bf16_f32 v27, v28, v29
	v_cvt_pk_bf16_f32 v28, v32, v33
	v_cvt_pk_bf16_f32 v29, v30, v31
	ds_write_b128 v240, v[26:29] offset:8192
	s_waitcnt lgkmcnt(0)
	s_barrier
	ds_read_b128 v[246:249], v241 offset:8192
	v_lshl_add_u64 v[244:245], v[20:21], 0, v[242:243]
	s_waitcnt lgkmcnt(0)
	global_store_dwordx4 v[244:245], v[246:249], off offset:256
	v_pk_fma_f32 v[30:31], v[108:109], s[44:45], v[4:5] op_sel_hi:[1,0,1]
	v_pk_fma_f32 v[32:33], v[106:107], s[44:45], v[2:3] op_sel_hi:[1,0,1]
	v_pk_fma_f32 v[28:29], v[116:117], s[44:45], v[8:9] op_sel_hi:[1,0,1]
	v_pk_fma_f32 v[26:27], v[114:115], s[44:45], v[6:7] op_sel_hi:[1,0,1]
	v_lshl_add_u64 v[20:21], v[18:19], 0, s[46:47]
	v_cvt_pk_bf16_f32 v26, v26, v27
	v_cvt_pk_bf16_f32 v27, v28, v29
	v_cvt_pk_bf16_f32 v28, v32, v33
	v_cvt_pk_bf16_f32 v29, v30, v31
	v_add_co_u32_e32 v30, vcc, s84, v18
	v_pk_fma_f32 v[32:33], v[94:95], s[44:45], v[10:11] op_sel_hi:[1,0,1]
	s_nop 0
	v_addc_co_u32_e32 v31, vcc, 0, v19, vcc
	ds_write_b128 v240, v[26:29]
	s_waitcnt lgkmcnt(0)
	s_barrier
	ds_read_b128 v[246:249], v241
	v_lshl_add_u64 v[244:245], v[30:31], 0, v[242:243]
	s_waitcnt lgkmcnt(0)
	global_store_dwordx4 v[244:245], v[246:249], off
	v_pk_fma_f32 v[30:31], v[96:97], s[44:45], v[12:13] op_sel_hi:[1,0,1]
	s_nop 0
	v_pk_fma_f32 v[28:29], v[104:105], s[44:45], v[16:17] op_sel_hi:[1,0,1]
	v_pk_fma_f32 v[26:27], v[102:103], s[44:45], v[14:15] op_sel_hi:[1,0,1]
	s_nop 0
	v_cvt_pk_bf16_f32 v26, v26, v27
	v_cvt_pk_bf16_f32 v27, v28, v29
	v_cvt_pk_bf16_f32 v28, v32, v33
	v_cvt_pk_bf16_f32 v29, v30, v31
	ds_write_b128 v240, v[26:29] offset:8192
	s_waitcnt lgkmcnt(0)
	s_barrier
	ds_read_b128 v[246:249], v241 offset:8192
	v_lshl_add_u64 v[244:245], v[20:21], 0, v[242:243]
	s_waitcnt lgkmcnt(0)
	global_store_dwordx4 v[244:245], v[246:249], off offset:256
	v_pk_fma_f32 v[30:31], v[92:93], s[44:45], v[4:5] op_sel_hi:[1,0,1]
	v_pk_fma_f32 v[32:33], v[90:91], s[44:45], v[2:3] op_sel_hi:[1,0,1]
	v_pk_fma_f32 v[28:29], v[100:101], s[44:45], v[8:9] op_sel_hi:[1,0,1]
	v_pk_fma_f32 v[26:27], v[98:99], s[44:45], v[6:7] op_sel_hi:[1,0,1]
	v_lshl_add_u64 v[20:21], v[18:19], 0, s[48:49]
	v_cvt_pk_bf16_f32 v26, v26, v27
	v_cvt_pk_bf16_f32 v27, v28, v29
	v_cvt_pk_bf16_f32 v28, v32, v33
	v_cvt_pk_bf16_f32 v29, v30, v31
	v_add_co_u32_e32 v30, vcc, s85, v18
	v_pk_fma_f32 v[6:7], v[82:83], s[44:45], v[6:7] op_sel_hi:[1,0,1]
	s_nop 0
	v_addc_co_u32_e32 v31, vcc, 0, v19, vcc
	ds_write_b128 v240, v[26:29]
	s_waitcnt lgkmcnt(0)
	s_barrier
	ds_read_b128 v[246:249], v241
	v_lshl_add_u64 v[244:245], v[30:31], 0, v[242:243]
	s_waitcnt lgkmcnt(0)
	global_store_dwordx4 v[244:245], v[246:249], off
	v_pk_fma_f32 v[30:31], v[80:81], s[44:45], v[12:13] op_sel_hi:[1,0,1]
	v_pk_fma_f32 v[32:33], v[78:79], s[44:45], v[10:11] op_sel_hi:[1,0,1]
	v_pk_fma_f32 v[26:27], v[86:87], s[44:45], v[14:15] op_sel_hi:[1,0,1]
	v_pk_fma_f32 v[28:29], v[88:89], s[44:45], v[16:17] op_sel_hi:[1,0,1]
	v_cvt_pk_bf16_f32 v26, v26, v27
	v_pk_fma_f32 v[8:9], v[84:85], s[44:45], v[8:9] op_sel_hi:[1,0,1]
	v_cvt_pk_bf16_f32 v27, v28, v29
	v_cvt_pk_bf16_f32 v28, v32, v33
	v_cvt_pk_bf16_f32 v29, v30, v31
	ds_write_b128 v240, v[26:29] offset:8192
	s_waitcnt lgkmcnt(0)
	s_barrier
	ds_read_b128 v[246:249], v241 offset:8192
	v_lshl_add_u64 v[244:245], v[20:21], 0, v[242:243]
	s_waitcnt lgkmcnt(0)
	global_store_dwordx4 v[244:245], v[246:249], off offset:256
	v_lshl_add_u64 v[20:21], v[18:19], 0, s[50:51]
	s_nop 0
	v_pk_fma_f32 v[26:27], v[76:77], s[44:45], v[4:5] op_sel_hi:[1,0,1]
	v_pk_fma_f32 v[4:5], v[74:75], s[44:45], v[2:3] op_sel_hi:[1,0,1]
	v_cvt_pk_bf16_f32 v2, v6, v7
	v_add_co_u32_e32 v6, vcc, s86, v18
	v_cvt_pk_bf16_f32 v3, v8, v9
	v_cvt_pk_bf16_f32 v4, v4, v5
	v_cvt_pk_bf16_f32 v5, v26, v27
	v_pk_fma_f32 v[8:9], v[66:67], s[44:45], v[10:11] op_sel_hi:[1,0,1]
	s_nop 0
	v_addc_co_u32_e32 v7, vcc, 0, v19, vcc
	ds_write_b128 v240, v[2:5]
	s_waitcnt lgkmcnt(0)
	s_barrier
	ds_read_b128 v[246:249], v241
	v_lshl_add_u64 v[244:245], v[6:7], 0, v[242:243]
	s_waitcnt lgkmcnt(0)
	global_store_dwordx4 v[244:245], v[246:249], off
	s_andn2_b64 vcc, exec, s[54:55]
	v_pk_fma_f32 v[6:7], v[68:69], s[44:45], v[12:13] op_sel_hi:[1,0,1]
	v_pk_fma_f32 v[4:5], v[72:73], s[44:45], v[16:17] op_sel_hi:[1,0,1]
	v_pk_fma_f32 v[2:3], v[70:71], s[44:45], v[14:15] op_sel_hi:[1,0,1]
	s_nop 0
	v_cvt_pk_bf16_f32 v2, v2, v3
	v_cvt_pk_bf16_f32 v3, v4, v5
	v_cvt_pk_bf16_f32 v4, v8, v9
	v_cvt_pk_bf16_f32 v5, v6, v7
	ds_write_b128 v240, v[2:5] offset:8192
	s_waitcnt lgkmcnt(0)
	s_barrier
	ds_read_b128 v[246:249], v241 offset:8192
	v_lshl_add_u64 v[244:245], v[20:21], 0, v[242:243]
	s_waitcnt lgkmcnt(0)
	s_barrier
	global_store_dwordx4 v[244:245], v[246:249], off offset:256
	s_cbranch_vccnz .LBB0_789
	s_andn2_b64 vcc, exec, s[28:29]
	s_cbranch_vccnz .LBB0_788
	s_barrier
	s_branch .LBB0_788

.LBB0_1500:
	v_lshrrev_b32_e32 v3, 1, v1
	v_and_b32_e32 v3, 24, v3
	v_and_b32_e32 v2, 15, v1
	v_lshlrev_b32_e32 v8, 1, v3
	s_add_u32 s16, s16, 0x35f00000
	v_lshl_or_b32 v198, s19, 6, v2
	v_lshl_or_b32 v2, v2, 6, v8
	v_lshlrev_b32_e32 v8, 2, v1
	s_addc_u32 s17, s17, 0
	s_lshl_b32 s19, s19, 13
	v_and_b32_e32 v8, 32, v8
	v_bitop3_b32 v9, v2, s19, v8 bitop3:0xde
	s_lshl_b32 s19, s36, 5
	s_and_b32 s38, s19, 0x60
	s_lshl_b32 s19, s38, 7
	s_add_u32 s36, s12, 0x80
	v_bitop3_b32 v2, v2, s19, v8 bitop3:0xde
	s_waitcnt vmcnt(2)
	s_barrier
	s_addc_u32 s37, s13, 0
	s_add_i32 s59, s55, 0x18000
	s_mov_b32 s19, m0
	s_mov_b32 m0, s59
	s_nop 0
	global_load_lds_dwordx4 v196, s[36:37]
	s_mov_b32 m0, s19
	s_add_i32 s60, s55, 0x1a000
	s_mov_b32 s19, m0
	s_mov_b32 m0, s60
	s_nop 0
	global_load_lds_dwordx4 v197, s[36:37]
	s_mov_b32 m0, s19
	s_add_u32 s36, s10, 0x80
	s_addc_u32 s37, s11, 0
	s_add_i32 s61, s55, 0x8000
	s_mov_b32 s19, m0
	s_mov_b32 m0, s61
	s_nop 0
	global_load_lds_dwordx4 v217, s[36:37]
	s_mov_b32 m0, s19
	s_add_i32 s62, s55, 0xa000
	s_mov_b32 s19, m0
	s_mov_b32 m0, s62
	s_nop 0
	global_load_lds_dwordx4 v219, s[36:37]
	s_mov_b32 m0, s19
	s_add_u32 s36, s12, 0x20080
	s_addc_u32 s37, s13, 0
	s_add_i32 s63, s55, 0x1c000
	s_mov_b32 s19, m0
	s_mov_b32 m0, s63
	s_nop 0
	global_load_lds_dwordx4 v196, s[36:37]
	s_mov_b32 m0, s19
	s_add_i32 s64, s55, 0x1e000
	s_mov_b32 s19, m0
	s_mov_b32 m0, s64
	s_nop 0
	global_load_lds_dwordx4 v197, s[36:37]
	s_mov_b32 m0, s19
	s_waitcnt vmcnt(6)
	s_add_i32 s36, s55, 0xc000
	s_cmpk_lt_u32 s18, 0x100
	v_add_u32_e32 v200, 0, v2
	s_cselect_b64 s[18:19], -1, 0
	v_or_b32_e32 v199, s38, v3
	v_add_u32_e32 v201, 0x10000, v200
	v_add_u32_e32 v202, 0x14000, v200
	v_add_u32_e32 v203, 0, v9
	v_mov_b32_e32 v204, s36
	v_mov_b32_e32 v205, s55
	v_mov_b32_e32 v206, s9
	v_mov_b32_e32 v207, s20
	v_mov_b32_e32 v209, s28
	v_mov_b32_e32 v210, s29
	s_mov_b32 s20, 0x3d000000
	s_mov_b64 s[28:29], 0x40000
	s_mov_b32 s65, 0x40000
	s_mov_b64 s[36:37], 0x48000
	s_mov_b32 s66, 0x48000
	s_mov_b64 s[38:39], 0x50000
	s_mov_b32 s67, 0x50000
	s_mov_b64 s[40:41], 0x58000
	s_mov_b32 s68, 0x58000
	v_mov_b64_e32 v[194:195], 0x1ff
	v_mov_b32_e32 v211, 1
	s_barrier
	s_waitcnt vmcnt(0)
	v_and_b32_e32 v250, 63, v0
	v_and_b32_e32 v251, 15, v250
	v_lshrrev_b32_e32 v252, 4, v250
	v_readfirstlane_b32 s99, v0
	s_lshr_b32 s99, s99, 6
	s_and_b32 s100, s99, 3
	s_lshr_b32 s101, s99, 2
	s_lshl_b32 s100, s100, 2
	v_add_u32_e32 v253, s100, v252
	v_xor_b32_e32 v254, v253, v251
	s_lshl_b32 s101, s101, 12
	s_add_i32 s101, s101, 0xc000
	v_lshlrev_b32_e32 v240, 8, v251
	v_lshl_add_u32 v240, v254, 4, v240
	v_add_u32_e32 v240, s101, v240
	v_lshlrev_b32_e32 v241, 8, v253
	v_lshl_add_u32 v241, v254, 4, v241
	v_add_u32_e32 v241, s101, v241
	v_sub_u32_e32 v242, v253, v251
	v_lshlrev_b32_e32 v242, 11, v242
	v_lshl_add_u32 v242, v251, 4, v242
	v_lshlrev_b32_e32 v244, 4, v253
	v_sub_u32_e32 v242, v242, v244
	v_ashrrev_i32_e32 v243, 31, v242
	s_branch .LBB0_1503

.LBB0_1528:
	v_lshl_add_u32 v12, s69, 8, v198
	v_lshl_or_b32 v2, s70, 8, v199
	v_ashrrev_i32_e32 v13, 31, v12
	v_ashrrev_i32_e32 v3, 31, v2
	v_lshlrev_b64 v[8:9], 11, v[12:13]
	v_lshl_add_u64 v[8:9], s[16:17], 0, v[8:9]
	v_lshlrev_b64 v[14:15], 1, v[2:3]
	v_lshl_add_u64 v[2:3], v[8:9], 0, v[14:15]
	v_pk_fma_f32 v[8:9], v[190:191], s[20:21], 0 op_sel_hi:[1,0,0]
	v_pk_fma_f32 v[10:11], v[192:193], s[20:21], 0 op_sel_hi:[1,0,0]
	v_cvt_pk_bf16_f32 v8, v8, v9
	v_pk_fma_f32 v[16:17], v[188:189], s[20:21], 0 op_sel_hi:[1,0,0]
	v_cvt_pk_bf16_f32 v9, v10, v11
	v_pk_fma_f32 v[18:19], v[186:187], s[20:21], 0 op_sel_hi:[1,0,0]
	v_pk_fma_f32 v[20:21], v[170:171], s[20:21], 0 op_sel_hi:[1,0,0]
	v_cvt_pk_bf16_f32 v10, v18, v19
	v_cvt_pk_bf16_f32 v11, v16, v17
	ds_write_b128 v240, v[8:11]
	s_waitcnt lgkmcnt(0)
	s_barrier
	ds_read_b128 v[246:249], v241
	v_lshl_add_u64 v[244:245], v[2:3], 0, v[242:243]
	s_waitcnt lgkmcnt(0)
	global_store_dwordx4 v[244:245], v[246:249], off
	v_pk_fma_f32 v[16:17], v[176:177], s[20:21], 0 op_sel_hi:[1,0,0]
	v_pk_fma_f32 v[18:19], v[174:175], s[20:21], 0 op_sel_hi:[1,0,0]
	v_pk_fma_f32 v[8:9], v[182:183], s[20:21], 0 op_sel_hi:[1,0,0]
	v_pk_fma_f32 v[10:11], v[184:185], s[20:21], 0 op_sel_hi:[1,0,0]
	v_cvt_pk_bf16_f32 v8, v8, v9
	s_nop 0
	v_cvt_pk_bf16_f32 v9, v10, v11
	v_cvt_pk_bf16_f32 v10, v18, v19
	v_cvt_pk_bf16_f32 v11, v16, v17
	ds_write_b128 v240, v[8:11] offset:8192
	s_waitcnt lgkmcnt(0)
	s_barrier
	ds_read_b128 v[246:249], v241 offset:8192
	v_lshl_add_u64 v[244:245], v[2:3], 0, v[242:243]
	s_waitcnt lgkmcnt(0)
	global_store_dwordx4 v[244:245], v[246:249], off offset:256
	v_pk_fma_f32 v[18:19], v[172:173], s[20:21], 0 op_sel_hi:[1,0,0]
	s_nop 0
	v_or_b32_e32 v8, 16, v12
	v_ashrrev_i32_e32 v9, 31, v8
	v_lshlrev_b64 v[8:9], 11, v[8:9]
	v_lshl_add_u64 v[8:9], s[16:17], 0, v[8:9]
	v_lshl_add_u64 v[16:17], v[8:9], 0, v[14:15]
	v_pk_fma_f32 v[8:9], v[178:179], s[20:21], 0 op_sel_hi:[1,0,0]
	v_pk_fma_f32 v[10:11], v[180:181], s[20:21], 0 op_sel_hi:[1,0,0]
	v_cvt_pk_bf16_f32 v8, v8, v9
	s_nop 0
	v_cvt_pk_bf16_f32 v9, v10, v11
	v_cvt_pk_bf16_f32 v10, v20, v21
	v_cvt_pk_bf16_f32 v11, v18, v19
	ds_write_b128 v240, v[8:11]
	s_waitcnt lgkmcnt(0)
	s_barrier
	ds_read_b128 v[246:249], v241
	v_lshl_add_u64 v[244:245], v[16:17], 0, v[242:243]
	s_waitcnt lgkmcnt(0)
	global_store_dwordx4 v[244:245], v[246:249], off
	v_pk_fma_f32 v[18:19], v[160:161], s[20:21], 0 op_sel_hi:[1,0,0]
	v_pk_fma_f32 v[20:21], v[158:159], s[20:21], 0 op_sel_hi:[1,0,0]
	v_pk_fma_f32 v[8:9], v[166:167], s[20:21], 0 op_sel_hi:[1,0,0]
	v_pk_fma_f32 v[10:11], v[168:169], s[20:21], 0 op_sel_hi:[1,0,0]
	v_cvt_pk_bf16_f32 v8, v8, v9
	s_nop 0
	v_cvt_pk_bf16_f32 v9, v10, v11
	v_cvt_pk_bf16_f32 v10, v20, v21
	v_cvt_pk_bf16_f32 v11, v18, v19
	ds_write_b128 v240, v[8:11] offset:8192
	s_waitcnt lgkmcnt(0)
	s_barrier
	ds_read_b128 v[246:249], v241 offset:8192
	v_lshl_add_u64 v[244:245], v[16:17], 0, v[242:243]
	s_waitcnt lgkmcnt(0)
	global_store_dwordx4 v[244:245], v[246:249], off offset:256
	v_pk_fma_f32 v[18:19], v[156:157], s[20:21], 0 op_sel_hi:[1,0,0]
	v_pk_fma_f32 v[20:21], v[154:155], s[20:21], 0 op_sel_hi:[1,0,0]
	v_or_b32_e32 v8, 32, v12
	v_ashrrev_i32_e32 v9, 31, v8
	v_lshlrev_b64 v[8:9], 11, v[8:9]
	v_lshl_add_u64 v[8:9], s[16:17], 0, v[8:9]
	v_lshl_add_u64 v[16:17], v[8:9], 0, v[14:15]
	v_pk_fma_f32 v[8:9], v[162:163], s[20:21], 0 op_sel_hi:[1,0,0]
	v_pk_fma_f32 v[10:11], v[164:165], s[20:21], 0 op_sel_hi:[1,0,0]
	v_cvt_pk_bf16_f32 v8, v8, v9
	s_nop 0
	v_cvt_pk_bf16_f32 v9, v10, v11
	v_cvt_pk_bf16_f32 v10, v20, v21
	v_cvt_pk_bf16_f32 v11, v18, v19
	ds_write_b128 v240, v[8:11]
	s_waitcnt lgkmcnt(0)
	s_barrier
	ds_read_b128 v[246:249], v241
	v_lshl_add_u64 v[244:245], v[16:17], 0, v[242:243]
	s_waitcnt lgkmcnt(0)
	global_store_dwordx4 v[244:245], v[246:249], off
	v_pk_fma_f32 v[18:19], v[144:145], s[20:21], 0 op_sel_hi:[1,0,0]
	v_pk_fma_f32 v[20:21], v[142:143], s[20:21], 0 op_sel_hi:[1,0,0]
	v_pk_fma_f32 v[8:9], v[150:151], s[20:21], 0 op_sel_hi:[1,0,0]
	v_pk_fma_f32 v[10:11], v[152:153], s[20:21], 0 op_sel_hi:[1,0,0]
	v_cvt_pk_bf16_f32 v8, v8, v9
	s_nop 0
	v_cvt_pk_bf16_f32 v9, v10, v11
	v_cvt_pk_bf16_f32 v10, v20, v21
	v_cvt_pk_bf16_f32 v11, v18, v19
	ds_write_b128 v240, v[8:11] offset:8192
	s_waitcnt lgkmcnt(0)
	s_barrier
	ds_read_b128 v[246:249], v241 offset:8192
	v_lshl_add_u64 v[244:245], v[16:17], 0, v[242:243]
	s_waitcnt lgkmcnt(0)
	global_store_dwordx4 v[244:245], v[246:249], off offset:256
	v_pk_fma_f32 v[16:17], v[138:139], s[20:21], 0 op_sel_hi:[1,0,0]
	s_nop 0
	v_or_b32_e32 v8, 48, v12
	v_ashrrev_i32_e32 v9, 31, v8
	v_lshlrev_b64 v[8:9], 11, v[8:9]
	v_lshl_add_u64 v[8:9], s[16:17], 0, v[8:9]
	v_lshl_add_u64 v[12:13], v[8:9], 0, v[14:15]
	v_pk_fma_f32 v[10:11], v[148:149], s[20:21], 0 op_sel_hi:[1,0,0]
	v_pk_fma_f32 v[8:9], v[146:147], s[20:21], 0 op_sel_hi:[1,0,0]
	v_pk_fma_f32 v[14:15], v[140:141], s[20:21], 0 op_sel_hi:[1,0,0]
	v_cvt_pk_bf16_f32 v8, v8, v9
	v_cvt_pk_bf16_f32 v9, v10, v11
	v_cvt_pk_bf16_f32 v10, v16, v17
	v_pk_fma_f32 v[16:17], v[130:131], s[20:21], 0 op_sel_hi:[1,0,0]
	v_cvt_pk_bf16_f32 v11, v14, v15
	ds_write_b128 v240, v[8:11]
	s_waitcnt lgkmcnt(0)
	s_barrier
	ds_read_b128 v[246:249], v241
	v_lshl_add_u64 v[244:245], v[12:13], 0, v[242:243]
	s_waitcnt lgkmcnt(0)
	global_store_dwordx4 v[244:245], v[246:249], off
	v_pk_fma_f32 v[14:15], v[132:133], s[20:21], 0 op_sel_hi:[1,0,0]
	s_nop 0
	v_pk_fma_f32 v[10:11], v[136:137], s[20:21], 0 op_sel_hi:[1,0,0]
	v_pk_fma_f32 v[8:9], v[134:135], s[20:21], 0 op_sel_hi:[1,0,0]
	s_nop 0
	v_cvt_pk_bf16_f32 v8, v8, v9
	v_cvt_pk_bf16_f32 v9, v10, v11
	v_cvt_pk_bf16_f32 v10, v16, v17
	v_cvt_pk_bf16_f32 v11, v14, v15
	ds_write_b128 v240, v[8:11] offset:8192
	s_waitcnt lgkmcnt(0)
	s_barrier
	ds_read_b128 v[246:249], v241 offset:8192
	v_lshl_add_u64 v[244:245], v[12:13], 0, v[242:243]
	s_waitcnt lgkmcnt(0)
	global_store_dwordx4 v[244:245], v[246:249], off offset:256
	v_pk_fma_f32 v[14:15], v[124:125], s[20:21], 0 op_sel_hi:[1,0,0]
	v_pk_fma_f32 v[16:17], v[122:123], s[20:21], 0 op_sel_hi:[1,0,0]
	v_pk_fma_f32 v[10:11], v[128:129], s[20:21], 0 op_sel_hi:[1,0,0]
	v_pk_fma_f32 v[8:9], v[126:127], s[20:21], 0 op_sel_hi:[1,0,0]
	v_lshl_add_u64 v[12:13], v[2:3], 0, s[28:29]
	v_cvt_pk_bf16_f32 v8, v8, v9
	v_cvt_pk_bf16_f32 v9, v10, v11
	v_cvt_pk_bf16_f32 v10, v16, v17
	v_cvt_pk_bf16_f32 v11, v14, v15
	v_add_co_u32_e32 v14, vcc, s65, v2
	v_pk_fma_f32 v[16:17], v[110:111], s[20:21], 0 op_sel_hi:[1,0,0]
	s_nop 0
	v_addc_co_u32_e32 v15, vcc, 0, v3, vcc
	ds_write_b128 v240, v[8:11]
	s_waitcnt lgkmcnt(0)
	s_barrier
	ds_read_b128 v[246:249], v241
	v_lshl_add_u64 v[244:245], v[14:15], 0, v[242:243]
	s_waitcnt lgkmcnt(0)
	global_store_dwordx4 v[244:245], v[246:249], off
	v_pk_fma_f32 v[14:15], v[112:113], s[20:21], 0 op_sel_hi:[1,0,0]
	s_nop 0
	v_pk_fma_f32 v[10:11], v[120:121], s[20:21], 0 op_sel_hi:[1,0,0]
	v_pk_fma_f32 v[8:9], v[118:119], s[20:21], 0 op_sel_hi:[1,0,0]
	s_nop 0
	v_cvt_pk_bf16_f32 v8, v8, v9
	v_cvt_pk_bf16_f32 v9, v10, v11
	v_cvt_pk_bf16_f32 v10, v16, v17
	v_cvt_pk_bf16_f32 v11, v14, v15
	ds_write_b128 v240, v[8:11] offset:8192
	s_waitcnt lgkmcnt(0)
	s_barrier
	ds_read_b128 v[246:249], v241 offset:8192
	v_lshl_add_u64 v[244:245], v[12:13], 0, v[242:243]
	s_waitcnt lgkmcnt(0)
	global_store_dwordx4 v[244:245], v[246:249], off offset:256
	v_pk_fma_f32 v[14:15], v[108:109], s[20:21], 0 op_sel_hi:[1,0,0]
	v_pk_fma_f32 v[16:17], v[106:107], s[20:21], 0 op_sel_hi:[1,0,0]
	v_pk_fma_f32 v[10:11], v[116:117], s[20:21], 0 op_sel_hi:[1,0,0]
	v_pk_fma_f32 v[8:9], v[114:115], s[20:21], 0 op_sel_hi:[1,0,0]
	v_lshl_add_u64 v[12:13], v[2:3], 0, s[36:37]
	v_cvt_pk_bf16_f32 v8, v8, v9
	v_cvt_pk_bf16_f32 v9, v10, v11
	v_cvt_pk_bf16_f32 v10, v16, v17
	v_cvt_pk_bf16_f32 v11, v14, v15
	v_add_co_u32_e32 v14, vcc, s66, v2
	v_pk_fma_f32 v[16:17], v[94:95], s[20:21], 0 op_sel_hi:[1,0,0]
	s_nop 0
	v_addc_co_u32_e32 v15, vcc, 0, v3, vcc
	ds_write_b128 v240, v[8:11]
	s_waitcnt lgkmcnt(0)
	s_barrier
	ds_read_b128 v[246:249], v241
	v_lshl_add_u64 v[244:245], v[14:15], 0, v[242:243]
	s_waitcnt lgkmcnt(0)
	global_store_dwordx4 v[244:245], v[246:249], off
	v_pk_fma_f32 v[14:15], v[96:97], s[20:21], 0 op_sel_hi:[1,0,0]
	s_nop 0
	v_pk_fma_f32 v[10:11], v[104:105], s[20:21], 0 op_sel_hi:[1,0,0]
	v_pk_fma_f32 v[8:9], v[102:103], s[20:21], 0 op_sel_hi:[1,0,0]
	s_nop 0
	v_cvt_pk_bf16_f32 v8, v8, v9
	v_cvt_pk_bf16_f32 v9, v10, v11
	v_cvt_pk_bf16_f32 v10, v16, v17
	v_cvt_pk_bf16_f32 v11, v14, v15
	ds_write_b128 v240, v[8:11] offset:8192
	s_waitcnt lgkmcnt(0)
	s_barrier
	ds_read_b128 v[246:249], v241 offset:8192
	v_lshl_add_u64 v[244:245], v[12:13], 0, v[242:243]
	s_waitcnt lgkmcnt(0)
	global_store_dwordx4 v[244:245], v[246:249], off offset:256
	v_pk_fma_f32 v[14:15], v[92:93], s[20:21], 0 op_sel_hi:[1,0,0]
	v_pk_fma_f32 v[16:17], v[90:91], s[20:21], 0 op_sel_hi:[1,0,0]
	v_pk_fma_f32 v[10:11], v[100:101], s[20:21], 0 op_sel_hi:[1,0,0]
	v_pk_fma_f32 v[8:9], v[98:99], s[20:21], 0 op_sel_hi:[1,0,0]
	v_lshl_add_u64 v[12:13], v[2:3], 0, s[38:39]
	v_cvt_pk_bf16_f32 v8, v8, v9
	v_cvt_pk_bf16_f32 v9, v10, v11
	v_cvt_pk_bf16_f32 v10, v16, v17
	v_cvt_pk_bf16_f32 v11, v14, v15
	v_add_co_u32_e32 v14, vcc, s67, v2
	v_pk_fma_f32 v[16:17], v[78:79], s[20:21], 0 op_sel_hi:[1,0,0]
	s_nop 0
	v_addc_co_u32_e32 v15, vcc, 0, v3, vcc
	ds_write_b128 v240, v[8:11]
	s_waitcnt lgkmcnt(0)
	s_barrier
	ds_read_b128 v[246:249], v241
	v_lshl_add_u64 v[244:245], v[14:15], 0, v[242:243]
	s_waitcnt lgkmcnt(0)
	global_store_dwordx4 v[244:245], v[246:249], off
	v_pk_fma_f32 v[14:15], v[80:81], s[20:21], 0 op_sel_hi:[1,0,0]
	s_nop 0
	v_pk_fma_f32 v[10:11], v[88:89], s[20:21], 0 op_sel_hi:[1,0,0]
	v_pk_fma_f32 v[8:9], v[86:87], s[20:21], 0 op_sel_hi:[1,0,0]
	s_nop 0
	v_cvt_pk_bf16_f32 v8, v8, v9
	v_cvt_pk_bf16_f32 v9, v10, v11
	v_cvt_pk_bf16_f32 v10, v16, v17
	v_cvt_pk_bf16_f32 v11, v14, v15
	ds_write_b128 v240, v[8:11] offset:8192
	s_waitcnt lgkmcnt(0)
	s_barrier
	ds_read_b128 v[246:249], v241 offset:8192
	v_lshl_add_u64 v[244:245], v[12:13], 0, v[242:243]
	s_waitcnt lgkmcnt(0)
	global_store_dwordx4 v[244:245], v[246:249], off offset:256
	v_lshl_add_u64 v[12:13], v[2:3], 0, s[40:41]
	v_add_co_u32_e32 v2, vcc, s68, v2
	v_pk_fma_f32 v[10:11], v[84:85], s[20:21], 0 op_sel_hi:[1,0,0]
	v_pk_fma_f32 v[8:9], v[82:83], s[20:21], 0 op_sel_hi:[1,0,0]
	v_pk_fma_f32 v[14:15], v[76:77], s[20:21], 0 op_sel_hi:[1,0,0]
	v_pk_fma_f32 v[16:17], v[74:75], s[20:21], 0 op_sel_hi:[1,0,0]
	v_cvt_pk_bf16_f32 v8, v8, v9
	v_cvt_pk_bf16_f32 v9, v10, v11
	v_addc_co_u32_e32 v3, vcc, 0, v3, vcc
	v_cvt_pk_bf16_f32 v10, v16, v17
	v_cvt_pk_bf16_f32 v11, v14, v15
	ds_write_b128 v240, v[8:11]
	s_waitcnt lgkmcnt(0)
	s_barrier
	ds_read_b128 v[246:249], v241
	v_lshl_add_u64 v[244:245], v[2:3], 0, v[242:243]
	s_waitcnt lgkmcnt(0)
	global_store_dwordx4 v[244:245], v[246:249], off
	s_andn2_b64 vcc, exec, s[42:43]
	s_mov_b64 s[42:43], -1
	v_pk_fma_f32 v[8:9], v[70:71], s[20:21], 0 op_sel_hi:[1,0,0]
	v_pk_fma_f32 v[10:11], v[66:67], s[20:21], 0 op_sel_hi:[1,0,0]
	v_pk_fma_f32 v[2:3], v[72:73], s[20:21], 0 op_sel_hi:[1,0,0]
	v_pk_fma_f32 v[14:15], v[68:69], s[20:21], 0 op_sel_hi:[1,0,0]
	v_cvt_pk_bf16_f32 v8, v8, v9
	v_cvt_pk_bf16_f32 v9, v2, v3
	v_cvt_pk_bf16_f32 v10, v10, v11
	s_nop 0
	v_cvt_pk_bf16_f32 v11, v14, v15
	ds_write_b128 v240, v[8:11] offset:8192
	s_waitcnt lgkmcnt(0)
	s_barrier
	ds_read_b128 v[246:249], v241 offset:8192
	v_lshl_add_u64 v[244:245], v[12:13], 0, v[242:243]
	s_waitcnt lgkmcnt(0)
	s_barrier
	global_store_dwordx4 v[244:245], v[246:249], off offset:256
	s_cbranch_vccnz .LBB0_1502
	s_andn2_b64 vcc, exec, s[14:15]
	s_cbranch_vccnz .LBB0_1501
	s_barrier
	s_branch .LBB0_1501

.LBB0_1863:
	s_add_u32 s28, s28, 0x4b400000
	s_addc_u32 s29, s29, 0
	v_lshrrev_b32_e32 v3, 1, v0
	s_add_u32 s72, s36, 0x20000
	v_and_b32_e32 v3, 24, v3
	s_addc_u32 s73, s37, 0
	v_and_b32_e32 v2, 15, v0
	v_lshlrev_b32_e32 v4, 1, v3
	s_add_u32 s36, s16, 0x80
	v_lshl_or_b32 v195, s38, 6, v2
	v_lshl_or_b32 v2, v2, 6, v4
	v_lshlrev_b32_e32 v4, 2, v0
	s_addc_u32 s37, s17, 0
	s_lshl_b32 s38, s38, 13
	v_and_b32_e32 v4, 32, v4
	v_bitop3_b32 v5, v2, s38, v4 bitop3:0xde
	s_lshl_b32 s38, s41, 5
	s_and_b32 s38, s38, 0x60
	s_lshl_b32 s41, s38, 7
	s_add_u32 s42, s18, 0x80
	v_bitop3_b32 v2, v2, s41, v4 bitop3:0xde
	s_waitcnt vmcnt(2)
	s_barrier
	s_addc_u32 s43, s19, 0
	s_add_i32 s74, s68, 0x18000
	s_mov_b32 s41, m0
	s_mov_b32 m0, s74
	s_nop 0
	global_load_lds_dwordx4 v1, s[42:43]
	s_mov_b32 m0, s41
	s_add_i32 s75, s68, 0x1a000
	s_mov_b32 s41, m0
	s_mov_b32 m0, s75
	s_nop 0
	global_load_lds_dwordx4 v194, s[42:43]
	s_mov_b32 m0, s41
	s_add_i32 s76, s68, 0x8000
	s_mov_b32 s41, m0
	s_mov_b32 m0, s76
	s_nop 0
	global_load_lds_dwordx4 v214, s[36:37]
	s_mov_b32 m0, s41
	s_add_i32 s77, s68, 0xa000
	s_mov_b32 s41, m0
	s_mov_b32 m0, s77
	s_nop 0
	global_load_lds_dwordx4 v216, s[36:37]
	s_mov_b32 m0, s41
	s_add_u32 s36, s18, 0x20080
	s_addc_u32 s37, s19, 0
	s_add_i32 s78, s68, 0x1c000
	s_mov_b32 s41, m0
	s_mov_b32 m0, s78
	s_nop 0
	global_load_lds_dwordx4 v1, s[36:37]
	s_mov_b32 m0, s41
	s_add_i32 s79, s68, 0x1e000
	s_mov_b32 s41, m0
	s_mov_b32 m0, s79
	s_nop 0
	global_load_lds_dwordx4 v194, s[36:37]
	s_mov_b32 m0, s41
	s_waitcnt vmcnt(6)
	s_add_i32 s41, s68, 0xc000
	s_cmpk_lt_u32 s30, 0x100
	v_add_u32_e32 v197, 0, v2
	s_cselect_b64 s[36:37], -1, 0
	v_or_b32_e32 v196, s38, v3
	v_add_u32_e32 v198, 0x10000, v197
	v_add_u32_e32 v199, 0x14000, v197
	v_add_u32_e32 v200, 0, v5
	v_mov_b32_e32 v201, s41
	v_mov_b32_e32 v202, s68
	v_mov_b32_e32 v203, s13
	v_mov_b32_e32 v204, s15
	v_mov_b32_e32 v205, s39
	v_mov_b32_e32 v206, s40
	s_mov_b32 s30, 0x3d000000
	s_mov_b64 s[38:39], 0x40000
	s_mov_b32 s80, 0x40000
	s_mov_b64 s[40:41], 0x48000
	s_mov_b32 s81, 0x48000
	s_mov_b64 s[42:43], 0x50000
	s_mov_b32 s82, 0x50000
	s_mov_b64 s[44:45], 0x58000
	s_mov_b32 s83, 0x58000
	v_mov_b32_e32 v207, 1
	s_barrier
	v_and_b32_e32 v250, 63, v0
	v_and_b32_e32 v251, 15, v250
	v_lshrrev_b32_e32 v252, 4, v250
	v_readfirstlane_b32 s99, v0
	s_lshr_b32 s99, s99, 6
	s_and_b32 s100, s99, 3
	s_lshr_b32 s101, s99, 2
	s_lshl_b32 s100, s100, 2
	v_add_u32_e32 v253, s100, v252
	v_xor_b32_e32 v254, v253, v251
	s_lshl_b32 s101, s101, 12
	s_add_i32 s101, s101, 0xc000
	v_lshlrev_b32_e32 v240, 8, v251
	v_lshl_add_u32 v240, v254, 4, v240
	v_add_u32_e32 v240, s101, v240
	v_lshlrev_b32_e32 v241, 8, v253
	v_lshl_add_u32 v241, v254, 4, v241
	v_add_u32_e32 v241, s101, v241
	v_sub_u32_e32 v242, v253, v251
	v_lshlrev_b32_e32 v242, 11, v242
	v_lshl_add_u32 v242, v251, 4, v242
	v_lshlrev_b32_e32 v244, 4, v253
	v_sub_u32_e32 v242, v242, v244
	v_ashrrev_i32_e32 v243, 31, v242
	s_branch .LBB0_1866

.LBB0_1891:
	v_lshl_or_b32 v18, s49, 8, v196
	s_ashr_i32 s49, s48, 31
	s_lshl_b64 s[48:49], s[48:49], 12
	s_add_u32 s48, s72, s48
	s_addc_u32 s49, s73, s49
	v_ashrrev_i32_e32 v19, 31, v18
	v_lshl_add_u64 v[2:3], v[18:19], 2, s[48:49]
	global_load_dwordx4 v[14:17], v[2:3], off
	global_load_dwordx4 v[10:13], v[2:3], off offset:16
	global_load_dwordx4 v[6:9], v[2:3], off offset:512
	s_nop 0
	global_load_dwordx4 v[2:5], v[2:3], off offset:528
	v_lshl_add_u32 v24, s84, 8, v195
	v_ashrrev_i32_e32 v25, 31, v24
	v_or_b32_e32 v26, 16, v24
	v_or_b32_e32 v28, 32, v24
	v_or_b32_e32 v30, 48, v24
	v_lshlrev_b64 v[24:25], 11, v[24:25]
	v_ashrrev_i32_e32 v27, 31, v26
	v_ashrrev_i32_e32 v29, 31, v28
	v_lshlrev_b64 v[32:33], 1, v[18:19]
	v_ashrrev_i32_e32 v31, 31, v30
	v_lshl_add_u64 v[18:19], s[28:29], 0, v[24:25]
	v_lshlrev_b64 v[24:25], 11, v[26:27]
	v_lshlrev_b64 v[26:27], 11, v[28:29]
	v_lshlrev_b64 v[28:29], 11, v[30:31]
	v_lshl_add_u64 v[24:25], s[28:29], 0, v[24:25]
	v_lshl_add_u64 v[26:27], s[28:29], 0, v[26:27]
	v_lshl_add_u64 v[28:29], s[28:29], 0, v[28:29]
	v_lshl_add_u64 v[30:31], v[24:25], 0, v[32:33]
	v_lshl_add_u64 v[34:35], v[26:27], 0, v[32:33]
	v_lshl_add_u64 v[18:19], v[18:19], 0, v[32:33]
	v_lshl_add_u64 v[28:29], v[28:29], 0, v[32:33]
	s_waitcnt vmcnt(3)
	v_pk_fma_f32 v[26:27], v[192:193], s[30:31], v[16:17] op_sel_hi:[1,0,1]
	v_pk_fma_f32 v[24:25], v[190:191], s[30:31], v[14:15] op_sel_hi:[1,0,1]
	s_waitcnt vmcnt(2)
	v_pk_fma_f32 v[32:33], v[188:189], s[30:31], v[12:13] op_sel_hi:[1,0,1]
	v_pk_fma_f32 v[36:37], v[186:187], s[30:31], v[10:11] op_sel_hi:[1,0,1]
	v_cvt_pk_bf16_f32 v24, v24, v25
	v_cvt_pk_bf16_f32 v25, v26, v27
	s_waitcnt vmcnt(1)
	v_pk_fma_f32 v[38:39], v[172:173], s[30:31], v[8:9] op_sel_hi:[1,0,1]
	v_cvt_pk_bf16_f32 v26, v36, v37
	v_cvt_pk_bf16_f32 v27, v32, v33
	v_pk_fma_f32 v[40:41], v[170:171], s[30:31], v[6:7] op_sel_hi:[1,0,1]
	s_waitcnt vmcnt(0)
	v_pk_fma_f32 v[42:43], v[164:165], s[30:31], v[4:5] op_sel_hi:[1,0,1]
	v_pk_fma_f32 v[44:45], v[162:163], s[30:31], v[2:3] op_sel_hi:[1,0,1]
	ds_write_b128 v240, v[24:27]
	s_waitcnt lgkmcnt(0)
	s_barrier
	ds_read_b128 v[246:249], v241
	v_lshl_add_u64 v[244:245], v[18:19], 0, v[242:243]
	s_waitcnt lgkmcnt(0)
	global_store_dwordx4 v[244:245], v[246:249], off
	v_pk_fma_f32 v[46:47], v[184:185], s[30:31], v[16:17] op_sel_hi:[1,0,1]
	v_pk_fma_f32 v[48:49], v[182:183], s[30:31], v[14:15] op_sel_hi:[1,0,1]
	v_cvt_pk_bf16_f32 v24, v40, v41
	v_cvt_pk_bf16_f32 v25, v38, v39
	v_cvt_pk_bf16_f32 v26, v44, v45
	v_cvt_pk_bf16_f32 v27, v42, v43
	v_pk_fma_f32 v[50:51], v[180:181], s[30:31], v[12:13] op_sel_hi:[1,0,1]
	v_pk_fma_f32 v[52:53], v[178:179], s[30:31], v[10:11] op_sel_hi:[1,0,1]
	ds_write_b128 v240, v[24:27] offset:8192
	s_waitcnt lgkmcnt(0)
	s_barrier
	ds_read_b128 v[246:249], v241 offset:8192
	v_lshl_add_u64 v[244:245], v[18:19], 0, v[242:243]
	s_waitcnt lgkmcnt(0)
	global_store_dwordx4 v[244:245], v[246:249], off offset:256
	v_pk_fma_f32 v[54:55], v[156:157], s[30:31], v[8:9] op_sel_hi:[1,0,1]
	v_pk_fma_f32 v[56:57], v[154:155], s[30:31], v[6:7] op_sel_hi:[1,0,1]
	v_cvt_pk_bf16_f32 v24, v48, v49
	v_cvt_pk_bf16_f32 v25, v46, v47
	v_cvt_pk_bf16_f32 v26, v52, v53
	v_cvt_pk_bf16_f32 v27, v50, v51
	v_pk_fma_f32 v[58:59], v[148:149], s[30:31], v[4:5] op_sel_hi:[1,0,1]
	v_pk_fma_f32 v[60:61], v[146:147], s[30:31], v[2:3] op_sel_hi:[1,0,1]
	ds_write_b128 v240, v[24:27]
	s_waitcnt lgkmcnt(0)
	s_barrier
	ds_read_b128 v[246:249], v241
	v_lshl_add_u64 v[244:245], v[30:31], 0, v[242:243]
	s_waitcnt lgkmcnt(0)
	global_store_dwordx4 v[244:245], v[246:249], off
	v_pk_fma_f32 v[62:63], v[176:177], s[30:31], v[16:17] op_sel_hi:[1,0,1]
	v_pk_fma_f32 v[64:65], v[174:175], s[30:31], v[14:15] op_sel_hi:[1,0,1]
	v_cvt_pk_bf16_f32 v24, v56, v57
	v_cvt_pk_bf16_f32 v25, v54, v55
	v_cvt_pk_bf16_f32 v26, v60, v61
	v_cvt_pk_bf16_f32 v27, v58, v59
	v_pk_fma_f32 v[146:147], v[168:169], s[30:31], v[12:13] op_sel_hi:[1,0,1]
	v_pk_fma_f32 v[148:149], v[166:167], s[30:31], v[10:11] op_sel_hi:[1,0,1]
	ds_write_b128 v240, v[24:27] offset:8192
	s_waitcnt lgkmcnt(0)
	s_barrier
	ds_read_b128 v[246:249], v241 offset:8192
	v_lshl_add_u64 v[244:245], v[30:31], 0, v[242:243]
	s_waitcnt lgkmcnt(0)
	global_store_dwordx4 v[244:245], v[246:249], off offset:256
	v_pk_fma_f32 v[144:145], v[144:145], s[30:31], v[8:9] op_sel_hi:[1,0,1]
	v_pk_fma_f32 v[142:143], v[142:143], s[30:31], v[6:7] op_sel_hi:[1,0,1]
	v_cvt_pk_bf16_f32 v24, v64, v65
	v_cvt_pk_bf16_f32 v25, v62, v63
	v_cvt_pk_bf16_f32 v26, v148, v149
	v_cvt_pk_bf16_f32 v27, v146, v147
	v_pk_fma_f32 v[140:141], v[140:141], s[30:31], v[4:5] op_sel_hi:[1,0,1]
	v_pk_fma_f32 v[138:139], v[138:139], s[30:31], v[2:3] op_sel_hi:[1,0,1]
	ds_write_b128 v240, v[24:27]
	s_waitcnt lgkmcnt(0)
	s_barrier
	ds_read_b128 v[246:249], v241
	v_lshl_add_u64 v[244:245], v[34:35], 0, v[242:243]
	s_waitcnt lgkmcnt(0)
	global_store_dwordx4 v[244:245], v[246:249], off
	v_pk_fma_f32 v[154:155], v[160:161], s[30:31], v[16:17] op_sel_hi:[1,0,1]
	v_pk_fma_f32 v[156:157], v[158:159], s[30:31], v[14:15] op_sel_hi:[1,0,1]
	v_cvt_pk_bf16_f32 v24, v142, v143
	v_cvt_pk_bf16_f32 v25, v144, v145
	v_cvt_pk_bf16_f32 v26, v138, v139
	v_cvt_pk_bf16_f32 v27, v140, v141
	v_pk_fma_f32 v[152:153], v[152:153], s[30:31], v[12:13] op_sel_hi:[1,0,1]
	v_pk_fma_f32 v[150:151], v[150:151], s[30:31], v[10:11] op_sel_hi:[1,0,1]
	ds_write_b128 v240, v[24:27] offset:8192
	s_waitcnt lgkmcnt(0)
	s_barrier
	ds_read_b128 v[246:249], v241 offset:8192
	v_lshl_add_u64 v[244:245], v[34:35], 0, v[242:243]
	s_waitcnt lgkmcnt(0)
	global_store_dwordx4 v[244:245], v[246:249], off offset:256
	v_pk_fma_f32 v[30:31], v[132:133], s[30:31], v[4:5] op_sel_hi:[1,0,1]
	v_pk_fma_f32 v[32:33], v[130:131], s[30:31], v[2:3] op_sel_hi:[1,0,1]
	v_cvt_pk_bf16_f32 v24, v156, v157
	v_cvt_pk_bf16_f32 v25, v154, v155
	v_cvt_pk_bf16_f32 v26, v150, v151
	v_cvt_pk_bf16_f32 v27, v152, v153
	ds_write_b128 v240, v[24:27]
	s_waitcnt lgkmcnt(0)
	s_barrier
	ds_read_b128 v[246:249], v241
	v_lshl_add_u64 v[244:245], v[28:29], 0, v[242:243]
	s_waitcnt lgkmcnt(0)
	global_store_dwordx4 v[244:245], v[246:249], off
	s_nop 1
	v_pk_fma_f32 v[26:27], v[136:137], s[30:31], v[8:9] op_sel_hi:[1,0,1]
	v_pk_fma_f32 v[24:25], v[134:135], s[30:31], v[6:7] op_sel_hi:[1,0,1]
	s_nop 0
	v_cvt_pk_bf16_f32 v24, v24, v25
	v_cvt_pk_bf16_f32 v25, v26, v27
	v_cvt_pk_bf16_f32 v26, v32, v33
	v_cvt_pk_bf16_f32 v27, v30, v31
	ds_write_b128 v240, v[24:27] offset:8192
	s_waitcnt lgkmcnt(0)
	s_barrier
	ds_read_b128 v[246:249], v241 offset:8192
	v_lshl_add_u64 v[244:245], v[28:29], 0, v[242:243]
	s_waitcnt lgkmcnt(0)
	global_store_dwordx4 v[244:245], v[246:249], off offset:256
	v_pk_fma_f32 v[30:31], v[124:125], s[30:31], v[12:13] op_sel_hi:[1,0,1]
	v_pk_fma_f32 v[32:33], v[122:123], s[30:31], v[10:11] op_sel_hi:[1,0,1]
	v_pk_fma_f32 v[26:27], v[128:129], s[30:31], v[16:17] op_sel_hi:[1,0,1]
	v_pk_fma_f32 v[24:25], v[126:127], s[30:31], v[14:15] op_sel_hi:[1,0,1]
	v_lshl_add_u64 v[28:29], v[18:19], 0, s[38:39]
	v_cvt_pk_bf16_f32 v24, v24, v25
	v_cvt_pk_bf16_f32 v25, v26, v27
	v_cvt_pk_bf16_f32 v26, v32, v33
	v_cvt_pk_bf16_f32 v27, v30, v31
	v_add_co_u32_e32 v30, vcc, s80, v18
	v_pk_fma_f32 v[32:33], v[110:111], s[30:31], v[2:3] op_sel_hi:[1,0,1]
	s_nop 0
	v_addc_co_u32_e32 v31, vcc, 0, v19, vcc
	ds_write_b128 v240, v[24:27]
	s_waitcnt lgkmcnt(0)
	s_barrier
	ds_read_b128 v[246:249], v241
	v_lshl_add_u64 v[244:245], v[30:31], 0, v[242:243]
	s_waitcnt lgkmcnt(0)
	global_store_dwordx4 v[244:245], v[246:249], off
	v_pk_fma_f32 v[30:31], v[112:113], s[30:31], v[4:5] op_sel_hi:[1,0,1]
	s_nop 0
	v_pk_fma_f32 v[26:27], v[120:121], s[30:31], v[8:9] op_sel_hi:[1,0,1]
	v_pk_fma_f32 v[24:25], v[118:119], s[30:31], v[6:7] op_sel_hi:[1,0,1]
	s_nop 0
	v_cvt_pk_bf16_f32 v24, v24, v25
	v_cvt_pk_bf16_f32 v25, v26, v27
	v_cvt_pk_bf16_f32 v26, v32, v33
	v_cvt_pk_bf16_f32 v27, v30, v31
	ds_write_b128 v240, v[24:27] offset:8192
	s_waitcnt lgkmcnt(0)
	s_barrier
	ds_read_b128 v[246:249], v241 offset:8192
	v_lshl_add_u64 v[244:245], v[28:29], 0, v[242:243]
	s_waitcnt lgkmcnt(0)
	global_store_dwordx4 v[244:245], v[246:249], off offset:256
	v_pk_fma_f32 v[30:31], v[108:109], s[30:31], v[12:13] op_sel_hi:[1,0,1]
	v_pk_fma_f32 v[32:33], v[106:107], s[30:31], v[10:11] op_sel_hi:[1,0,1]
	v_pk_fma_f32 v[26:27], v[116:117], s[30:31], v[16:17] op_sel_hi:[1,0,1]
	v_pk_fma_f32 v[24:25], v[114:115], s[30:31], v[14:15] op_sel_hi:[1,0,1]
	v_lshl_add_u64 v[28:29], v[18:19], 0, s[40:41]
	v_cvt_pk_bf16_f32 v24, v24, v25
	v_cvt_pk_bf16_f32 v25, v26, v27
	v_cvt_pk_bf16_f32 v26, v32, v33
	v_cvt_pk_bf16_f32 v27, v30, v31
	v_add_co_u32_e32 v30, vcc, s81, v18
	v_pk_fma_f32 v[32:33], v[94:95], s[30:31], v[2:3] op_sel_hi:[1,0,1]
	s_nop 0
	v_addc_co_u32_e32 v31, vcc, 0, v19, vcc
	ds_write_b128 v240, v[24:27]
	s_waitcnt lgkmcnt(0)
	s_barrier
	ds_read_b128 v[246:249], v241
	v_lshl_add_u64 v[244:245], v[30:31], 0, v[242:243]
	s_waitcnt lgkmcnt(0)
	global_store_dwordx4 v[244:245], v[246:249], off
	v_pk_fma_f32 v[30:31], v[96:97], s[30:31], v[4:5] op_sel_hi:[1,0,1]
	s_nop 0
	v_pk_fma_f32 v[26:27], v[104:105], s[30:31], v[8:9] op_sel_hi:[1,0,1]
	v_pk_fma_f32 v[24:25], v[102:103], s[30:31], v[6:7] op_sel_hi:[1,0,1]
	s_nop 0
	v_cvt_pk_bf16_f32 v24, v24, v25
	v_cvt_pk_bf16_f32 v25, v26, v27
	v_cvt_pk_bf16_f32 v26, v32, v33
	v_cvt_pk_bf16_f32 v27, v30, v31
	ds_write_b128 v240, v[24:27] offset:8192
	s_waitcnt lgkmcnt(0)
	s_barrier
	ds_read_b128 v[246:249], v241 offset:8192
	v_lshl_add_u64 v[244:245], v[28:29], 0, v[242:243]
	s_waitcnt lgkmcnt(0)
	global_store_dwordx4 v[244:245], v[246:249], off offset:256
	v_pk_fma_f32 v[30:31], v[92:93], s[30:31], v[12:13] op_sel_hi:[1,0,1]
	v_pk_fma_f32 v[32:33], v[90:91], s[30:31], v[10:11] op_sel_hi:[1,0,1]
	v_pk_fma_f32 v[26:27], v[100:101], s[30:31], v[16:17] op_sel_hi:[1,0,1]
	v_pk_fma_f32 v[24:25], v[98:99], s[30:31], v[14:15] op_sel_hi:[1,0,1]
	v_lshl_add_u64 v[28:29], v[18:19], 0, s[42:43]
	v_cvt_pk_bf16_f32 v24, v24, v25
	v_cvt_pk_bf16_f32 v25, v26, v27
	v_cvt_pk_bf16_f32 v26, v32, v33
	v_cvt_pk_bf16_f32 v27, v30, v31
	v_add_co_u32_e32 v30, vcc, s82, v18
	v_pk_fma_f32 v[32:33], v[78:79], s[30:31], v[2:3] op_sel_hi:[1,0,1]
	s_nop 0
	v_addc_co_u32_e32 v31, vcc, 0, v19, vcc
	ds_write_b128 v240, v[24:27]
	s_waitcnt lgkmcnt(0)
	s_barrier
	ds_read_b128 v[246:249], v241
	v_lshl_add_u64 v[244:245], v[30:31], 0, v[242:243]
	s_waitcnt lgkmcnt(0)
	global_store_dwordx4 v[244:245], v[246:249], off
	v_pk_fma_f32 v[30:31], v[80:81], s[30:31], v[4:5] op_sel_hi:[1,0,1]
	v_pk_fma_f32 v[14:15], v[82:83], s[30:31], v[14:15] op_sel_hi:[1,0,1]
	v_pk_fma_f32 v[26:27], v[88:89], s[30:31], v[8:9] op_sel_hi:[1,0,1]
	v_pk_fma_f32 v[24:25], v[86:87], s[30:31], v[6:7] op_sel_hi:[1,0,1]
	v_pk_fma_f32 v[16:17], v[84:85], s[30:31], v[16:17] op_sel_hi:[1,0,1]
	v_cvt_pk_bf16_f32 v24, v24, v25
	v_cvt_pk_bf16_f32 v25, v26, v27
	v_cvt_pk_bf16_f32 v26, v32, v33
	v_cvt_pk_bf16_f32 v27, v30, v31
	ds_write_b128 v240, v[24:27] offset:8192
	s_waitcnt lgkmcnt(0)
	s_barrier
	ds_read_b128 v[246:249], v241 offset:8192
	v_lshl_add_u64 v[244:245], v[28:29], 0, v[242:243]
	s_waitcnt lgkmcnt(0)
	global_store_dwordx4 v[244:245], v[246:249], off offset:256
	v_pk_fma_f32 v[8:9], v[72:73], s[30:31], v[8:9] op_sel_hi:[1,0,1]
	v_pk_fma_f32 v[6:7], v[70:71], s[30:31], v[6:7] op_sel_hi:[1,0,1]
	v_pk_fma_f32 v[26:27], v[76:77], s[30:31], v[12:13] op_sel_hi:[1,0,1]
	v_pk_fma_f32 v[12:13], v[74:75], s[30:31], v[10:11] op_sel_hi:[1,0,1]
	v_cvt_pk_bf16_f32 v10, v14, v15
	v_add_co_u32_e32 v14, vcc, s83, v18
	v_cvt_pk_bf16_f32 v11, v16, v17
	v_lshl_add_u64 v[24:25], v[18:19], 0, s[44:45]
	s_nop 0
	v_addc_co_u32_e32 v15, vcc, 0, v19, vcc
	v_cvt_pk_bf16_f32 v12, v12, v13
	v_cvt_pk_bf16_f32 v13, v26, v27
	ds_write_b128 v240, v[10:13]
	s_waitcnt lgkmcnt(0)
	s_barrier
	ds_read_b128 v[246:249], v241
	v_lshl_add_u64 v[244:245], v[14:15], 0, v[242:243]
	s_waitcnt lgkmcnt(0)
	global_store_dwordx4 v[244:245], v[246:249], off
	s_andn2_b64 vcc, exec, s[46:47]
	s_mov_b64 s[46:47], -1
	v_pk_fma_f32 v[10:11], v[68:69], s[30:31], v[4:5] op_sel_hi:[1,0,1]
	v_pk_fma_f32 v[4:5], v[66:67], s[30:31], v[2:3] op_sel_hi:[1,0,1]
	v_cvt_pk_bf16_f32 v2, v6, v7
	v_cvt_pk_bf16_f32 v3, v8, v9
	s_nop 0
	v_cvt_pk_bf16_f32 v4, v4, v5
	v_cvt_pk_bf16_f32 v5, v10, v11
	ds_write_b128 v240, v[2:5] offset:8192
	s_waitcnt lgkmcnt(0)
	s_barrier
	ds_read_b128 v[246:249], v241 offset:8192
	v_lshl_add_u64 v[244:245], v[24:25], 0, v[242:243]
	s_waitcnt lgkmcnt(0)
	s_barrier
	global_store_dwordx4 v[244:245], v[246:249], off offset:256
	s_cbranch_vccnz .LBB0_1865
	s_andn2_b64 vcc, exec, s[20:21]
	s_cbranch_vccnz .LBB0_1864
	s_barrier
	s_branch .LBB0_1864
